# plus: GEMM load segments: M0 write before the address add (no s_nop), merged vmcnt+lgkmcnt wait, saddr-form LDS-DMA where the address is scalar base + lane offset
# baseline (speedup 1.0000x reference)
.LBB0_514:
	s_add_u32 s22, s82, s92
	s_addc_u32 s23, s83, s93
	s_add_u32 s24, s22, 0x100
	s_addc_u32 s25, s23, 0
	s_add_u32 s58, s3, s92
	s_addc_u32 s59, s2, s93
	s_add_i32 vcc_lo, 0, 0x10000
	s_cmpk_eq_i32 s92, 0xf00
	s_cselect_b64 s[26:27], -1, 0
	s_and_b64 s[22:23], s[26:27], exec
	s_cselect_b32 s25, s67, s25
	s_cselect_b32 s24, s75, s24
	s_cselect_b32 s23, s95, s59
	s_cselect_b32 s22, s29, s58
	s_add_i32 vcc_hi, 0, 0x14000
	v_add_u32_e32 v130, vcc_lo, v223
	v_add_u32_e32 v142, vcc_hi, v223
	ds_read_b128 v[146:149], v130
	ds_read_b128 v[150:153], v130 offset:1024
	ds_read_b128 v[154:157], v130 offset:2048
	ds_read_b128 v[158:161], v130 offset:3072
	ds_read_b128 v[130:133], v142
	ds_read_b128 v[134:137], v142 offset:1024
	ds_read_b128 v[138:141], v142 offset:2048
	ds_read_b128 v[142:145], v142 offset:3072
	v_lshl_add_u64 v[214:215], v[210:211], 0, s[92:93]
	s_add_i32 m0, s81, 0xc000
	ds_read_b128 v[162:165], v224
	ds_read_b128 v[166:169], v224 offset:1024
	ds_read_b128 v[170:173], v224 offset:2048
	ds_read_b128 v[174:177], v224 offset:3072
	ds_read_b128 v[178:181], v224 offset:4096
	ds_read_b128 v[182:185], v224 offset:5120
	ds_read_b128 v[186:189], v224 offset:6144
	ds_read_b128 v[190:193], v224 offset:7168
	global_load_lds_dwordx4 v[214:215], off
	s_add_i32 m0, s81, 0xe000
	v_lshl_add_u64 v[214:215], v[212:213], 0, s[92:93]
	global_load_lds_dwordx4 v[214:215], off
	s_waitcnt vmcnt(8) lgkmcnt(0)
	s_barrier
	v_mfma_f32_16x16x32_bf16 v[124:127], v[146:149], v[162:165], v[124:127]
	v_mfma_f32_16x16x32_bf16 v[120:123], v[154:157], v[162:165], v[120:123]
	v_mfma_f32_16x16x32_bf16 v[116:119], v[146:149], v[170:173], v[116:119]
	v_mfma_f32_16x16x32_bf16 v[108:111], v[154:157], v[170:173], v[108:111]
	v_mfma_f32_16x16x32_bf16 v[100:103], v[146:149], v[178:181], v[100:103]
	v_mfma_f32_16x16x32_bf16 v[92:95], v[154:157], v[178:181], v[92:95]
	v_mfma_f32_16x16x32_bf16 v[84:87], v[146:149], v[186:189], v[84:87]
	v_mfma_f32_16x16x32_bf16 v[76:79], v[154:157], v[186:189], v[76:79]
	v_mfma_f32_16x16x32_bf16 v[124:127], v[150:153], v[166:169], v[124:127]
	v_mfma_f32_16x16x32_bf16 v[120:123], v[158:161], v[166:169], v[120:123]
	v_mfma_f32_16x16x32_bf16 v[116:119], v[150:153], v[174:177], v[116:119]
	v_mfma_f32_16x16x32_bf16 v[108:111], v[158:161], v[174:177], v[108:111]
	v_mfma_f32_16x16x32_bf16 v[100:103], v[150:153], v[182:185], v[100:103]
	v_mfma_f32_16x16x32_bf16 v[92:95], v[158:161], v[182:185], v[92:95]
	v_mfma_f32_16x16x32_bf16 v[84:87], v[150:153], v[190:193], v[84:87]
	v_mfma_f32_16x16x32_bf16 v[76:79], v[158:161], v[190:193], v[76:79]
	v_mfma_f32_16x16x32_bf16 v[112:115], v[130:133], v[162:165], v[112:115]
	v_mfma_f32_16x16x32_bf16 v[104:107], v[138:141], v[162:165], v[104:107]
	v_mfma_f32_16x16x32_bf16 v[96:99], v[130:133], v[170:173], v[96:99]
	v_mfma_f32_16x16x32_bf16 v[88:91], v[138:141], v[170:173], v[88:91]
	v_mfma_f32_16x16x32_bf16 v[80:83], v[130:133], v[178:181], v[80:83]
	v_mfma_f32_16x16x32_bf16 v[72:75], v[138:141], v[178:181], v[72:75]
	v_mfma_f32_16x16x32_bf16 v[68:71], v[130:133], v[186:189], v[68:71]
	v_mfma_f32_16x16x32_bf16 v[64:67], v[138:141], v[186:189], v[64:67]
	v_mfma_f32_16x16x32_bf16 v[112:115], v[134:137], v[166:169], v[112:115]
	v_mfma_f32_16x16x32_bf16 v[104:107], v[142:145], v[166:169], v[104:107]
	v_mfma_f32_16x16x32_bf16 v[96:99], v[134:137], v[174:177], v[96:99]
	v_mfma_f32_16x16x32_bf16 v[88:91], v[142:145], v[174:177], v[88:91]
	v_mfma_f32_16x16x32_bf16 v[80:83], v[134:137], v[182:185], v[80:83]
	v_mfma_f32_16x16x32_bf16 v[72:75], v[142:145], v[182:185], v[72:75]
	v_mfma_f32_16x16x32_bf16 v[68:71], v[134:137], v[190:193], v[68:71]
	v_mfma_f32_16x16x32_bf16 v[64:67], v[142:145], v[190:193], v[64:67]
	s_barrier
	s_add_i32 s58, vcc_lo, s28
	v_lshl_add_u64 v[214:215], s[22:23], 0, v[200:201]
	s_mov_b32 m0, s58
	ds_read_b128 v[186:189], v224 offset:16384
	ds_read_b128 v[190:193], v224 offset:17408
	ds_read_b128 v[178:181], v224 offset:18432
	ds_read_b128 v[182:185], v224 offset:19456
	ds_read_b128 v[170:173], v224 offset:20480
	ds_read_b128 v[174:177], v224 offset:21504
	ds_read_b128 v[162:165], v224 offset:22528
	ds_read_b128 v[166:169], v224 offset:23552
	global_load_lds_dwordx4 v[214:215], off
	s_add_i32 m0, s58, 0x2000
	s_add_u32 s58, s22, 0x80000
	v_lshl_add_u64 v[216:217], s[22:23], 0, v[204:205]
	s_addc_u32 s59, s23, 0
	s_add_i32 vcc_lo, vcc_hi, s28
	global_load_lds_dwordx4 v[216:217], off
	s_mov_b32 m0, vcc_lo
	v_lshl_add_u64 v[220:221], s[24:25], 0, v[202:203]
	global_load_lds_dwordx4 v200, s[58:59]
	s_add_i32 m0, vcc_lo, 0x2000
	v_cndmask_b32_e64 v194, 0, 1, s[96:97]
	global_load_lds_dwordx4 v204, s[58:59]
	v_lshl_add_u64 v[218:219], s[24:25], 0, v[198:199]
	s_mov_b32 m0, s81
	v_cmp_ne_u32_e64 s[58:59], 1, v194
	global_load_lds_dwordx4 v[218:219], off
	s_mov_b32 m0, s88
	s_andn2_b64 vcc, exec, s[96:97]
	global_load_lds_dwordx4 v[220:221], off
	s_waitcnt vmcnt(8) lgkmcnt(0)
	s_barrier
	s_cbranch_vccnz .LBB0_516
	s_waitcnt lgkmcnt(0)
	v_mfma_f32_16x16x32_bf16 v[60:63], v[146:149], v[186:189], v[60:63]
	v_mfma_f32_16x16x32_bf16 v[56:59], v[154:157], v[186:189], v[56:59]
	v_mfma_f32_16x16x32_bf16 v[44:47], v[146:149], v[178:181], v[44:47]
	v_mfma_f32_16x16x32_bf16 v[40:43], v[154:157], v[178:181], v[40:43]
	v_mfma_f32_16x16x32_bf16 v[28:31], v[146:149], v[170:173], v[28:31]
	v_mfma_f32_16x16x32_bf16 v[24:27], v[154:157], v[170:173], v[24:27]
	v_mfma_f32_16x16x32_bf16 v[12:15], v[146:149], v[162:165], v[12:15]
	v_mfma_f32_16x16x32_bf16 v[8:11], v[154:157], v[162:165], v[8:11]
	v_mfma_f32_16x16x32_bf16 v[60:63], v[150:153], v[190:193], v[60:63]
	v_mfma_f32_16x16x32_bf16 v[56:59], v[158:161], v[190:193], v[56:59]
	v_mfma_f32_16x16x32_bf16 v[44:47], v[150:153], v[182:185], v[44:47]
	v_mfma_f32_16x16x32_bf16 v[40:43], v[158:161], v[182:185], v[40:43]
	v_mfma_f32_16x16x32_bf16 v[28:31], v[150:153], v[174:177], v[28:31]
	v_mfma_f32_16x16x32_bf16 v[24:27], v[158:161], v[174:177], v[24:27]
	v_mfma_f32_16x16x32_bf16 v[12:15], v[150:153], v[166:169], v[12:15]
	v_mfma_f32_16x16x32_bf16 v[8:11], v[158:161], v[166:169], v[8:11]
	v_mfma_f32_16x16x32_bf16 v[52:55], v[130:133], v[186:189], v[52:55]
	v_mfma_f32_16x16x32_bf16 v[48:51], v[138:141], v[186:189], v[48:51]
	v_mfma_f32_16x16x32_bf16 v[36:39], v[130:133], v[178:181], v[36:39]
	v_mfma_f32_16x16x32_bf16 v[32:35], v[138:141], v[178:181], v[32:35]
	v_mfma_f32_16x16x32_bf16 v[20:23], v[130:133], v[170:173], v[20:23]
	v_mfma_f32_16x16x32_bf16 v[16:19], v[138:141], v[170:173], v[16:19]
	v_mfma_f32_16x16x32_bf16 v[4:7], v[130:133], v[162:165], v[4:7]
	v_mfma_f32_16x16x32_bf16 v[0:3], v[138:141], v[162:165], v[0:3]
	v_mfma_f32_16x16x32_bf16 v[52:55], v[134:137], v[190:193], v[52:55]
	v_mfma_f32_16x16x32_bf16 v[48:51], v[142:145], v[190:193], v[48:51]
	v_mfma_f32_16x16x32_bf16 v[36:39], v[134:137], v[182:185], v[36:39]
	v_mfma_f32_16x16x32_bf16 v[32:35], v[142:145], v[182:185], v[32:35]
	v_mfma_f32_16x16x32_bf16 v[20:23], v[134:137], v[174:177], v[20:23]
	v_mfma_f32_16x16x32_bf16 v[16:19], v[142:145], v[174:177], v[16:19]
	v_mfma_f32_16x16x32_bf16 v[4:7], v[134:137], v[166:169], v[4:7]
	v_mfma_f32_16x16x32_bf16 v[0:3], v[142:145], v[166:169], v[0:3]
.LBB0_516:
	s_barrier
	s_add_i32 vcc_lo, 0, 0x18000
	s_add_i32 vcc_hi, 0, 0x1c000
	v_add_u32_e32 v130, vcc_lo, v223
	v_add_u32_e32 v142, vcc_hi, v223
	ds_read_b128 v[146:149], v130
	ds_read_b128 v[150:153], v130 offset:1024
	ds_read_b128 v[154:157], v130 offset:2048
	ds_read_b128 v[158:161], v130 offset:3072
	ds_read_b128 v[130:133], v142
	ds_read_b128 v[134:137], v142 offset:1024
	ds_read_b128 v[138:141], v142 offset:2048
	ds_read_b128 v[142:145], v142 offset:3072
	s_and_b64 s[26:27], s[26:27], exec
	s_cselect_b32 s27, s72, s86
	s_cselect_b32 s26, 0, s87
	s_add_u32 s24, s24, s27
	s_addc_u32 s25, s25, s26
	s_mov_b32 m0, s89
	ds_read_b128 v[162:165], v224 offset:32768
	ds_read_b128 v[166:169], v224 offset:33792
	ds_read_b128 v[170:173], v224 offset:34816
	ds_read_b128 v[174:177], v224 offset:35840
	ds_read_b128 v[178:181], v224 offset:36864
	ds_read_b128 v[182:185], v224 offset:37888
	ds_read_b128 v[186:189], v224 offset:38912
	ds_read_b128 v[190:193], v224 offset:39936
	global_load_lds_dwordx4 v198, s[24:25]
	s_mov_b32 m0, s90
	s_nop 0
	global_load_lds_dwordx4 v202, s[24:25]
	s_waitcnt vmcnt(8) lgkmcnt(0)
	s_barrier
	v_mfma_f32_16x16x32_bf16 v[124:127], v[146:149], v[162:165], v[124:127]
	v_mfma_f32_16x16x32_bf16 v[120:123], v[154:157], v[162:165], v[120:123]
	v_mfma_f32_16x16x32_bf16 v[116:119], v[146:149], v[170:173], v[116:119]
	v_mfma_f32_16x16x32_bf16 v[108:111], v[154:157], v[170:173], v[108:111]
	v_mfma_f32_16x16x32_bf16 v[100:103], v[146:149], v[178:181], v[100:103]
	v_mfma_f32_16x16x32_bf16 v[92:95], v[154:157], v[178:181], v[92:95]
	v_mfma_f32_16x16x32_bf16 v[84:87], v[146:149], v[186:189], v[84:87]
	v_mfma_f32_16x16x32_bf16 v[76:79], v[154:157], v[186:189], v[76:79]
	v_mfma_f32_16x16x32_bf16 v[124:127], v[150:153], v[166:169], v[124:127]
	v_mfma_f32_16x16x32_bf16 v[120:123], v[158:161], v[166:169], v[120:123]
	v_mfma_f32_16x16x32_bf16 v[116:119], v[150:153], v[174:177], v[116:119]
	v_mfma_f32_16x16x32_bf16 v[108:111], v[158:161], v[174:177], v[108:111]
	v_mfma_f32_16x16x32_bf16 v[100:103], v[150:153], v[182:185], v[100:103]
	v_mfma_f32_16x16x32_bf16 v[92:95], v[158:161], v[182:185], v[92:95]
	v_mfma_f32_16x16x32_bf16 v[84:87], v[150:153], v[190:193], v[84:87]
	v_mfma_f32_16x16x32_bf16 v[76:79], v[158:161], v[190:193], v[76:79]
	v_mfma_f32_16x16x32_bf16 v[112:115], v[130:133], v[162:165], v[112:115]
	v_mfma_f32_16x16x32_bf16 v[104:107], v[138:141], v[162:165], v[104:107]
	v_mfma_f32_16x16x32_bf16 v[96:99], v[130:133], v[170:173], v[96:99]
	v_mfma_f32_16x16x32_bf16 v[88:91], v[138:141], v[170:173], v[88:91]
	v_mfma_f32_16x16x32_bf16 v[80:83], v[130:133], v[178:181], v[80:83]
	v_mfma_f32_16x16x32_bf16 v[72:75], v[138:141], v[178:181], v[72:75]
	v_mfma_f32_16x16x32_bf16 v[68:71], v[130:133], v[186:189], v[68:71]
	v_mfma_f32_16x16x32_bf16 v[64:67], v[138:141], v[186:189], v[64:67]
	v_mfma_f32_16x16x32_bf16 v[112:115], v[134:137], v[166:169], v[112:115]
	v_mfma_f32_16x16x32_bf16 v[104:107], v[142:145], v[166:169], v[104:107]
	v_mfma_f32_16x16x32_bf16 v[96:99], v[134:137], v[174:177], v[96:99]
	v_mfma_f32_16x16x32_bf16 v[88:91], v[142:145], v[174:177], v[88:91]
	v_mfma_f32_16x16x32_bf16 v[80:83], v[134:137], v[182:185], v[80:83]
	v_mfma_f32_16x16x32_bf16 v[72:75], v[142:145], v[182:185], v[72:75]
	v_mfma_f32_16x16x32_bf16 v[68:71], v[134:137], v[190:193], v[68:71]
	v_mfma_f32_16x16x32_bf16 v[64:67], v[142:145], v[190:193], v[64:67]
	s_barrier
	s_add_i32 s24, vcc_lo, s28
	v_lshl_add_u64 v[214:215], v[214:215], 0, s[42:43]
	s_mov_b32 m0, s24
	ds_read_b128 v[186:189], v224 offset:49152
	ds_read_b128 v[190:193], v224 offset:50176
	ds_read_b128 v[178:181], v224 offset:51200
	ds_read_b128 v[182:185], v224 offset:52224
	ds_read_b128 v[170:173], v224 offset:53248
	ds_read_b128 v[174:177], v224 offset:54272
	ds_read_b128 v[162:165], v224 offset:55296
	ds_read_b128 v[166:169], v224 offset:56320
	global_load_lds_dwordx4 v[214:215], off
	s_add_i32 m0, s24, 0x2000
	s_add_u32 s22, s22, 0x80080
	v_lshl_add_u64 v[214:215], v[216:217], 0, s[42:43]
	s_addc_u32 s23, s23, 0
	s_add_i32 s24, vcc_hi, s28
	global_load_lds_dwordx4 v[214:215], off
	s_mov_b32 m0, s24
	s_and_b64 vcc, exec, s[58:59]
	global_load_lds_dwordx4 v200, s[22:23]
	s_add_i32 m0, s24, 0x2000
	s_nop 0
	global_load_lds_dwordx4 v204, s[22:23]
	s_mov_b32 m0, s91
	v_lshl_add_u64 v[214:215], v[218:219], 0, s[42:43]
	global_load_lds_dwordx4 v[214:215], off
	s_mov_b32 m0, s94
	v_lshl_add_u64 v[214:215], v[220:221], 0, s[42:43]
	global_load_lds_dwordx4 v[214:215], off
	s_waitcnt vmcnt(8) lgkmcnt(0)
	s_barrier
	s_cbranch_vccnz .LBB0_513
	s_waitcnt lgkmcnt(0)
	v_mfma_f32_16x16x32_bf16 v[60:63], v[146:149], v[186:189], v[60:63]
	v_mfma_f32_16x16x32_bf16 v[56:59], v[154:157], v[186:189], v[56:59]
	v_mfma_f32_16x16x32_bf16 v[44:47], v[146:149], v[178:181], v[44:47]
	v_mfma_f32_16x16x32_bf16 v[40:43], v[154:157], v[178:181], v[40:43]
	v_mfma_f32_16x16x32_bf16 v[28:31], v[146:149], v[170:173], v[28:31]
	v_mfma_f32_16x16x32_bf16 v[24:27], v[154:157], v[170:173], v[24:27]
	v_mfma_f32_16x16x32_bf16 v[12:15], v[146:149], v[162:165], v[12:15]
	v_mfma_f32_16x16x32_bf16 v[8:11], v[154:157], v[162:165], v[8:11]
	v_mfma_f32_16x16x32_bf16 v[60:63], v[150:153], v[190:193], v[60:63]
	v_mfma_f32_16x16x32_bf16 v[56:59], v[158:161], v[190:193], v[56:59]
	v_mfma_f32_16x16x32_bf16 v[44:47], v[150:153], v[182:185], v[44:47]
	v_mfma_f32_16x16x32_bf16 v[40:43], v[158:161], v[182:185], v[40:43]
	v_mfma_f32_16x16x32_bf16 v[28:31], v[150:153], v[174:177], v[28:31]
	v_mfma_f32_16x16x32_bf16 v[24:27], v[158:161], v[174:177], v[24:27]
	v_mfma_f32_16x16x32_bf16 v[12:15], v[150:153], v[166:169], v[12:15]
	v_mfma_f32_16x16x32_bf16 v[8:11], v[158:161], v[166:169], v[8:11]
	v_mfma_f32_16x16x32_bf16 v[52:55], v[130:133], v[186:189], v[52:55]
	v_mfma_f32_16x16x32_bf16 v[48:51], v[138:141], v[186:189], v[48:51]
	v_mfma_f32_16x16x32_bf16 v[36:39], v[130:133], v[178:181], v[36:39]
	v_mfma_f32_16x16x32_bf16 v[32:35], v[138:141], v[178:181], v[32:35]
	v_mfma_f32_16x16x32_bf16 v[20:23], v[130:133], v[170:173], v[20:23]
	v_mfma_f32_16x16x32_bf16 v[16:19], v[138:141], v[170:173], v[16:19]
	v_mfma_f32_16x16x32_bf16 v[4:7], v[130:133], v[162:165], v[4:7]
	v_mfma_f32_16x16x32_bf16 v[0:3], v[138:141], v[162:165], v[0:3]
	v_mfma_f32_16x16x32_bf16 v[52:55], v[134:137], v[190:193], v[52:55]
	v_mfma_f32_16x16x32_bf16 v[48:51], v[142:145], v[190:193], v[48:51]
	v_mfma_f32_16x16x32_bf16 v[36:39], v[134:137], v[182:185], v[36:39]
	v_mfma_f32_16x16x32_bf16 v[32:35], v[142:145], v[182:185], v[32:35]
	v_mfma_f32_16x16x32_bf16 v[20:23], v[134:137], v[174:177], v[20:23]
	v_mfma_f32_16x16x32_bf16 v[16:19], v[142:145], v[174:177], v[16:19]
	v_mfma_f32_16x16x32_bf16 v[4:7], v[134:137], v[166:169], v[4:7]
	v_mfma_f32_16x16x32_bf16 v[0:3], v[142:145], v[166:169], v[0:3]
	s_branch .LBB0_513

.LBB0_725:
	s_add_u32 s2, s64, 0xfffe0080
	s_addc_u32 s3, s65, -1
	s_add_i32 s29, 0, 0x10000
	s_cmp_eq_u32 s66, 4
	s_cselect_b32 s25, s61, s3
	s_cselect_b32 s24, s60, s2
	v_add_u32_e32 v145, s29, v143
	s_cselect_b32 s23, s63, s17
	s_cselect_b32 s22, s62, s15
	s_add_i32 s30, 0, 0x14000
	ds_read_b128 v[146:149], v145
	ds_read_b128 v[150:153], v145 offset:1024
	ds_read_b128 v[154:157], v145 offset:2048
	ds_read_b128 v[158:161], v145 offset:3072
	v_add_u32_e32 v145, s30, v143
	ds_read_b128 v[162:165], v145
	ds_read_b128 v[166:169], v145 offset:1024
	ds_read_b128 v[170:173], v145 offset:2048
	ds_read_b128 v[174:177], v145 offset:3072
	s_add_i32 m0, s53, 0xc000
	ds_read_b128 v[178:181], v144
	ds_read_b128 v[182:185], v144 offset:1024
	ds_read_b128 v[186:189], v144 offset:2048
	ds_read_b128 v[190:193], v144 offset:3072
	ds_read_b128 v[198:201], v144 offset:4096
	ds_read_b128 v[202:205], v144 offset:5120
	ds_read_b128 v[206:209], v144 offset:6144
	ds_read_b128 v[210:213], v144 offset:7168
	global_load_lds_dwordx4 v138, s[64:65]
	s_add_i32 m0, s53, 0xe000
	s_nop 0
	global_load_lds_dwordx4 v140, s[64:65]
	s_waitcnt vmcnt(8) lgkmcnt(0)
	s_barrier
	v_mfma_f32_16x16x32_bf16 v[124:127], v[146:149], v[178:181], v[124:127]
	v_mfma_f32_16x16x32_bf16 v[120:123], v[154:157], v[178:181], v[120:123]
	v_mfma_f32_16x16x32_bf16 v[116:119], v[146:149], v[186:189], v[116:119]
	v_mfma_f32_16x16x32_bf16 v[108:111], v[154:157], v[186:189], v[108:111]
	v_mfma_f32_16x16x32_bf16 v[100:103], v[146:149], v[198:201], v[100:103]
	v_mfma_f32_16x16x32_bf16 v[92:95], v[154:157], v[198:201], v[92:95]
	v_mfma_f32_16x16x32_bf16 v[84:87], v[146:149], v[206:209], v[84:87]
	v_mfma_f32_16x16x32_bf16 v[76:79], v[154:157], v[206:209], v[76:79]
	v_mfma_f32_16x16x32_bf16 v[124:127], v[150:153], v[182:185], v[124:127]
	v_mfma_f32_16x16x32_bf16 v[120:123], v[158:161], v[182:185], v[120:123]
	v_mfma_f32_16x16x32_bf16 v[116:119], v[150:153], v[190:193], v[116:119]
	v_mfma_f32_16x16x32_bf16 v[108:111], v[158:161], v[190:193], v[108:111]
	v_mfma_f32_16x16x32_bf16 v[100:103], v[150:153], v[202:205], v[100:103]
	v_mfma_f32_16x16x32_bf16 v[92:95], v[158:161], v[202:205], v[92:95]
	v_mfma_f32_16x16x32_bf16 v[84:87], v[150:153], v[210:213], v[84:87]
	v_mfma_f32_16x16x32_bf16 v[76:79], v[158:161], v[210:213], v[76:79]
	v_mfma_f32_16x16x32_bf16 v[112:115], v[162:165], v[178:181], v[112:115]
	v_mfma_f32_16x16x32_bf16 v[104:107], v[170:173], v[178:181], v[104:107]
	v_mfma_f32_16x16x32_bf16 v[96:99], v[162:165], v[186:189], v[96:99]
	v_mfma_f32_16x16x32_bf16 v[88:91], v[170:173], v[186:189], v[88:91]
	v_mfma_f32_16x16x32_bf16 v[80:83], v[162:165], v[198:201], v[80:83]
	v_mfma_f32_16x16x32_bf16 v[72:75], v[170:173], v[198:201], v[72:75]
	v_mfma_f32_16x16x32_bf16 v[68:71], v[162:165], v[206:209], v[68:71]
	v_mfma_f32_16x16x32_bf16 v[64:67], v[170:173], v[206:209], v[64:67]
	v_mfma_f32_16x16x32_bf16 v[112:115], v[166:169], v[182:185], v[112:115]
	v_mfma_f32_16x16x32_bf16 v[104:107], v[174:177], v[182:185], v[104:107]
	v_mfma_f32_16x16x32_bf16 v[96:99], v[166:169], v[190:193], v[96:99]
	v_mfma_f32_16x16x32_bf16 v[88:91], v[174:177], v[190:193], v[88:91]
	v_mfma_f32_16x16x32_bf16 v[80:83], v[166:169], v[202:205], v[80:83]
	v_mfma_f32_16x16x32_bf16 v[72:75], v[174:177], v[202:205], v[72:75]
	v_mfma_f32_16x16x32_bf16 v[68:71], v[166:169], v[210:213], v[68:71]
	v_mfma_f32_16x16x32_bf16 v[64:67], v[174:177], v[210:213], v[64:67]
	s_barrier
	s_add_i32 s2, s29, s39
	v_lshl_add_u64 v[214:215], s[22:23], 0, v[134:135]
	s_mov_b32 m0, s2
	ds_read_b128 v[178:181], v144 offset:16384
	ds_read_b128 v[182:185], v144 offset:17408
	ds_read_b128 v[186:189], v144 offset:18432
	ds_read_b128 v[190:193], v144 offset:19456
	ds_read_b128 v[198:201], v144 offset:20480
	ds_read_b128 v[202:205], v144 offset:21504
	ds_read_b128 v[206:209], v144 offset:22528
	ds_read_b128 v[210:213], v144 offset:23552
	global_load_lds_dwordx4 v[214:215], off
	s_add_i32 m0, s2, 0x2000
	s_add_u32 s2, s22, 0x20000
	v_lshl_add_u64 v[216:217], s[22:23], 0, v[130:131]
	s_addc_u32 s3, s23, 0
	s_add_i32 s29, s30, s39
	global_load_lds_dwordx4 v[216:217], off
	s_mov_b32 m0, s29
	v_lshl_add_u64 v[220:221], s[24:25], 0, v[132:133]
	global_load_lds_dwordx4 v134, s[2:3]
	s_add_i32 m0, s29, 0x2000
	s_nop 0
	global_load_lds_dwordx4 v130, s[2:3]
	s_mov_b32 m0, s53
	v_lshl_add_u64 v[218:219], s[24:25], 0, v[136:137]
	global_load_lds_dwordx4 v[218:219], off
	s_mov_b32 m0, s68
	s_nop 0
	global_load_lds_dwordx4 v[220:221], off
	s_waitcnt vmcnt(8) lgkmcnt(0)
	s_barrier
	v_mfma_f32_16x16x32_bf16 v[60:63], v[146:149], v[178:181], v[60:63]
	v_mfma_f32_16x16x32_bf16 v[56:59], v[154:157], v[178:181], v[56:59]
	v_mfma_f32_16x16x32_bf16 v[52:55], v[146:149], v[186:189], v[52:55]
	v_mfma_f32_16x16x32_bf16 v[44:47], v[154:157], v[186:189], v[44:47]
	v_mfma_f32_16x16x32_bf16 v[36:39], v[146:149], v[198:201], v[36:39]
	v_mfma_f32_16x16x32_bf16 v[28:31], v[154:157], v[198:201], v[28:31]
	v_mfma_f32_16x16x32_bf16 v[20:23], v[146:149], v[206:209], v[20:23]
	v_mfma_f32_16x16x32_bf16 v[12:15], v[154:157], v[206:209], v[12:15]
	v_mfma_f32_16x16x32_bf16 v[60:63], v[150:153], v[182:185], v[60:63]
	v_mfma_f32_16x16x32_bf16 v[56:59], v[158:161], v[182:185], v[56:59]
	v_mfma_f32_16x16x32_bf16 v[52:55], v[150:153], v[190:193], v[52:55]
	v_mfma_f32_16x16x32_bf16 v[44:47], v[158:161], v[190:193], v[44:47]
	v_mfma_f32_16x16x32_bf16 v[36:39], v[150:153], v[202:205], v[36:39]
	v_mfma_f32_16x16x32_bf16 v[28:31], v[158:161], v[202:205], v[28:31]
	v_mfma_f32_16x16x32_bf16 v[20:23], v[150:153], v[210:213], v[20:23]
	v_mfma_f32_16x16x32_bf16 v[12:15], v[158:161], v[210:213], v[12:15]
	v_mfma_f32_16x16x32_bf16 v[48:51], v[162:165], v[178:181], v[48:51]
	v_mfma_f32_16x16x32_bf16 v[40:43], v[170:173], v[178:181], v[40:43]
	v_mfma_f32_16x16x32_bf16 v[32:35], v[162:165], v[186:189], v[32:35]
	v_mfma_f32_16x16x32_bf16 v[24:27], v[170:173], v[186:189], v[24:27]
	v_mfma_f32_16x16x32_bf16 v[16:19], v[162:165], v[198:201], v[16:19]
	v_mfma_f32_16x16x32_bf16 v[8:11], v[170:173], v[198:201], v[8:11]
	v_mfma_f32_16x16x32_bf16 v[4:7], v[162:165], v[206:209], v[4:7]
	v_mfma_f32_16x16x32_bf16 v[0:3], v[170:173], v[206:209], v[0:3]
	v_mfma_f32_16x16x32_bf16 v[48:51], v[166:169], v[182:185], v[48:51]
	v_mfma_f32_16x16x32_bf16 v[40:43], v[174:177], v[182:185], v[40:43]
	v_mfma_f32_16x16x32_bf16 v[32:35], v[166:169], v[190:193], v[32:35]
	v_mfma_f32_16x16x32_bf16 v[24:27], v[174:177], v[190:193], v[24:27]
	v_mfma_f32_16x16x32_bf16 v[16:19], v[166:169], v[202:205], v[16:19]
	v_mfma_f32_16x16x32_bf16 v[8:11], v[174:177], v[202:205], v[8:11]
	v_mfma_f32_16x16x32_bf16 v[4:7], v[166:169], v[210:213], v[4:7]
	v_mfma_f32_16x16x32_bf16 v[0:3], v[174:177], v[210:213], v[0:3]
	s_barrier
	s_add_i32 s29, 0, 0x18000
	v_add_u32_e32 v145, s29, v143
	s_add_i32 s30, 0, 0x1c000
	ds_read_b128 v[146:149], v145
	ds_read_b128 v[150:153], v145 offset:1024
	ds_read_b128 v[154:157], v145 offset:2048
	ds_read_b128 v[158:161], v145 offset:3072
	v_add_u32_e32 v145, s30, v143
	ds_read_b128 v[162:165], v145
	ds_read_b128 v[166:169], v145 offset:1024
	ds_read_b128 v[170:173], v145 offset:2048
	ds_read_b128 v[174:177], v145 offset:3072
	s_add_u32 s2, s24, 0x20000
	s_addc_u32 s3, s25, 0
	s_mov_b32 m0, s69
	ds_read_b128 v[178:181], v144 offset:32768
	ds_read_b128 v[182:185], v144 offset:33792
	ds_read_b128 v[186:189], v144 offset:34816
	ds_read_b128 v[190:193], v144 offset:35840
	ds_read_b128 v[198:201], v144 offset:36864
	ds_read_b128 v[202:205], v144 offset:37888
	ds_read_b128 v[206:209], v144 offset:38912
	ds_read_b128 v[210:213], v144 offset:39936
	global_load_lds_dwordx4 v136, s[2:3]
	s_mov_b32 m0, s70
	s_nop 0
	global_load_lds_dwordx4 v132, s[2:3]
	s_waitcnt vmcnt(8) lgkmcnt(0)
	s_barrier
	v_mfma_f32_16x16x32_bf16 v[124:127], v[146:149], v[178:181], v[124:127]
	v_mfma_f32_16x16x32_bf16 v[120:123], v[154:157], v[178:181], v[120:123]
	v_mfma_f32_16x16x32_bf16 v[116:119], v[146:149], v[186:189], v[116:119]
	v_mfma_f32_16x16x32_bf16 v[108:111], v[154:157], v[186:189], v[108:111]
	v_mfma_f32_16x16x32_bf16 v[100:103], v[146:149], v[198:201], v[100:103]
	v_mfma_f32_16x16x32_bf16 v[92:95], v[154:157], v[198:201], v[92:95]
	v_mfma_f32_16x16x32_bf16 v[84:87], v[146:149], v[206:209], v[84:87]
	v_mfma_f32_16x16x32_bf16 v[76:79], v[154:157], v[206:209], v[76:79]
	v_mfma_f32_16x16x32_bf16 v[124:127], v[150:153], v[182:185], v[124:127]
	v_mfma_f32_16x16x32_bf16 v[120:123], v[158:161], v[182:185], v[120:123]
	v_mfma_f32_16x16x32_bf16 v[116:119], v[150:153], v[190:193], v[116:119]
	v_mfma_f32_16x16x32_bf16 v[108:111], v[158:161], v[190:193], v[108:111]
	v_mfma_f32_16x16x32_bf16 v[100:103], v[150:153], v[202:205], v[100:103]
	v_mfma_f32_16x16x32_bf16 v[92:95], v[158:161], v[202:205], v[92:95]
	v_mfma_f32_16x16x32_bf16 v[84:87], v[150:153], v[210:213], v[84:87]
	v_mfma_f32_16x16x32_bf16 v[76:79], v[158:161], v[210:213], v[76:79]
	v_mfma_f32_16x16x32_bf16 v[112:115], v[162:165], v[178:181], v[112:115]
	v_mfma_f32_16x16x32_bf16 v[104:107], v[170:173], v[178:181], v[104:107]
	v_mfma_f32_16x16x32_bf16 v[96:99], v[162:165], v[186:189], v[96:99]
	v_mfma_f32_16x16x32_bf16 v[88:91], v[170:173], v[186:189], v[88:91]
	v_mfma_f32_16x16x32_bf16 v[80:83], v[162:165], v[198:201], v[80:83]
	v_mfma_f32_16x16x32_bf16 v[72:75], v[170:173], v[198:201], v[72:75]
	v_mfma_f32_16x16x32_bf16 v[68:71], v[162:165], v[206:209], v[68:71]
	v_mfma_f32_16x16x32_bf16 v[64:67], v[170:173], v[206:209], v[64:67]
	v_mfma_f32_16x16x32_bf16 v[112:115], v[166:169], v[182:185], v[112:115]
	v_mfma_f32_16x16x32_bf16 v[104:107], v[174:177], v[182:185], v[104:107]
	v_mfma_f32_16x16x32_bf16 v[96:99], v[166:169], v[190:193], v[96:99]
	v_mfma_f32_16x16x32_bf16 v[88:91], v[174:177], v[190:193], v[88:91]
	v_mfma_f32_16x16x32_bf16 v[80:83], v[166:169], v[202:205], v[80:83]
	v_mfma_f32_16x16x32_bf16 v[72:75], v[174:177], v[202:205], v[72:75]
	v_mfma_f32_16x16x32_bf16 v[68:71], v[166:169], v[210:213], v[68:71]
	v_mfma_f32_16x16x32_bf16 v[64:67], v[174:177], v[210:213], v[64:67]
	s_barrier
	s_add_i32 s2, s29, s39
	v_lshl_add_u64 v[214:215], v[214:215], 0, s[42:43]
	s_mov_b32 m0, s2
	ds_read_b128 v[178:181], v144 offset:49152
	ds_read_b128 v[182:185], v144 offset:50176
	ds_read_b128 v[186:189], v144 offset:51200
	ds_read_b128 v[190:193], v144 offset:52224
	ds_read_b128 v[198:201], v144 offset:53248
	ds_read_b128 v[202:205], v144 offset:54272
	ds_read_b128 v[206:209], v144 offset:55296
	ds_read_b128 v[210:213], v144 offset:56320
	global_load_lds_dwordx4 v[214:215], off
	s_add_i32 m0, s2, 0x2000
	s_add_u32 s2, s22, 0x20080
	v_lshl_add_u64 v[214:215], v[216:217], 0, s[42:43]
	s_addc_u32 s3, s23, 0
	s_add_i32 s22, s30, s39
	global_load_lds_dwordx4 v[214:215], off
	s_mov_b32 m0, s22
	s_nop 0
	global_load_lds_dwordx4 v134, s[2:3]
	s_add_i32 m0, s22, 0x2000
	s_nop 0
	global_load_lds_dwordx4 v130, s[2:3]
	s_mov_b32 m0, s71
	v_lshl_add_u64 v[214:215], v[218:219], 0, s[42:43]
	global_load_lds_dwordx4 v[214:215], off
	s_mov_b32 m0, s74
	v_lshl_add_u64 v[214:215], v[220:221], 0, s[42:43]
	global_load_lds_dwordx4 v[214:215], off
	s_waitcnt vmcnt(8) lgkmcnt(0)
	s_barrier
	v_mfma_f32_16x16x32_bf16 v[60:63], v[146:149], v[178:181], v[60:63]
	v_mfma_f32_16x16x32_bf16 v[56:59], v[154:157], v[178:181], v[56:59]
	v_mfma_f32_16x16x32_bf16 v[52:55], v[146:149], v[186:189], v[52:55]
	v_mfma_f32_16x16x32_bf16 v[44:47], v[154:157], v[186:189], v[44:47]
	v_mfma_f32_16x16x32_bf16 v[36:39], v[146:149], v[198:201], v[36:39]
	v_mfma_f32_16x16x32_bf16 v[28:31], v[154:157], v[198:201], v[28:31]
	v_mfma_f32_16x16x32_bf16 v[20:23], v[146:149], v[206:209], v[20:23]
	v_mfma_f32_16x16x32_bf16 v[12:15], v[154:157], v[206:209], v[12:15]
	v_mfma_f32_16x16x32_bf16 v[60:63], v[150:153], v[182:185], v[60:63]
	v_mfma_f32_16x16x32_bf16 v[56:59], v[158:161], v[182:185], v[56:59]
	v_mfma_f32_16x16x32_bf16 v[52:55], v[150:153], v[190:193], v[52:55]
	v_mfma_f32_16x16x32_bf16 v[44:47], v[158:161], v[190:193], v[44:47]
	v_mfma_f32_16x16x32_bf16 v[36:39], v[150:153], v[202:205], v[36:39]
	v_mfma_f32_16x16x32_bf16 v[28:31], v[158:161], v[202:205], v[28:31]
	v_mfma_f32_16x16x32_bf16 v[20:23], v[150:153], v[210:213], v[20:23]
	v_mfma_f32_16x16x32_bf16 v[12:15], v[158:161], v[210:213], v[12:15]
	v_mfma_f32_16x16x32_bf16 v[48:51], v[162:165], v[178:181], v[48:51]
	v_mfma_f32_16x16x32_bf16 v[40:43], v[170:173], v[178:181], v[40:43]
	v_mfma_f32_16x16x32_bf16 v[32:35], v[162:165], v[186:189], v[32:35]
	v_mfma_f32_16x16x32_bf16 v[24:27], v[170:173], v[186:189], v[24:27]
	v_mfma_f32_16x16x32_bf16 v[16:19], v[162:165], v[198:201], v[16:19]
	v_mfma_f32_16x16x32_bf16 v[8:11], v[170:173], v[198:201], v[8:11]
	v_mfma_f32_16x16x32_bf16 v[4:7], v[162:165], v[206:209], v[4:7]
	v_mfma_f32_16x16x32_bf16 v[0:3], v[170:173], v[206:209], v[0:3]
	v_mfma_f32_16x16x32_bf16 v[48:51], v[166:169], v[182:185], v[48:51]
	v_mfma_f32_16x16x32_bf16 v[40:43], v[174:177], v[182:185], v[40:43]
	v_mfma_f32_16x16x32_bf16 v[32:35], v[166:169], v[190:193], v[32:35]
	v_mfma_f32_16x16x32_bf16 v[24:27], v[174:177], v[190:193], v[24:27]
	v_mfma_f32_16x16x32_bf16 v[16:19], v[166:169], v[202:205], v[16:19]
	v_mfma_f32_16x16x32_bf16 v[8:11], v[174:177], v[202:205], v[8:11]
	v_mfma_f32_16x16x32_bf16 v[4:7], v[166:169], v[210:213], v[4:7]
	v_mfma_f32_16x16x32_bf16 v[0:3], v[174:177], v[210:213], v[0:3]
	s_barrier
	s_add_i32 s66, s66, 2
	s_add_u32 s64, s64, 0x100
	s_addc_u32 s65, s65, 0
	s_add_u32 s15, s15, 0x100
	s_addc_u32 s17, s17, 0
	s_cmp_gt_u32 s66, 5
	s_cbranch_scc0 .LBB0_725
	s_and_b64 vcc, exec, s[10:11]
	s_cbranch_vccz .LBB0_728
	s_barrier

.LBB0_969:
	s_add_u32 s24, s18, s92
	s_addc_u32 s25, s19, s93
	s_add_u32 s60, s24, 0x100
	s_addc_u32 s61, s25, 0
	s_add_u32 s81, s2, s92
	s_addc_u32 s84, s29, s93
	s_add_i32 vcc_lo, 0, 0x10000
	s_cmpk_eq_i32 s92, 0xf00
	s_cselect_b64 s[26:27], -1, 0
	s_and_b64 s[24:25], s[26:27], exec
	s_cselect_b32 s25, s15, s61
	s_cselect_b32 s24, s17, s60
	s_waitcnt lgkmcnt(0)
	v_add_u32_e32 v104, vcc_lo, v234
	s_cselect_b32 s85, s67, s84
	s_cselect_b32 s84, s3, s81
	s_add_i32 s81, 0, 0x14000
	ds_read_b128 v[162:165], v104
	ds_read_b128 v[166:169], v104 offset:1024
	ds_read_b128 v[170:173], v104 offset:2048
	ds_read_b128 v[174:177], v104 offset:3072
	v_add_u32_e32 v104, s81, v234
	ds_read_b128 v[146:149], v104
	ds_read_b128 v[150:153], v104 offset:1024
	ds_read_b128 v[154:157], v104 offset:2048
	ds_read_b128 v[158:161], v104 offset:3072
	v_lshl_add_u64 v[104:105], v[208:209], 0, s[92:93]
	s_add_i32 m0, s53, 0xc000
	ds_read_b128 v[178:181], v236
	ds_read_b128 v[182:185], v236 offset:1024
	ds_read_b128 v[186:189], v236 offset:2048
	ds_read_b128 v[190:193], v236 offset:3072
	ds_read_b128 v[210:213], v236 offset:4096
	ds_read_b128 v[214:217], v236 offset:5120
	ds_read_b128 v[218:221], v236 offset:6144
	ds_read_b128 v[222:225], v236 offset:7168
	global_load_lds_dwordx4 v[104:105], off
	s_add_i32 m0, s53, 0xe000
	v_lshl_add_u64 v[104:105], v[206:207], 0, s[92:93]
	global_load_lds_dwordx4 v[104:105], off
	s_waitcnt vmcnt(8) lgkmcnt(0)
	s_barrier
	v_mfma_f32_16x16x32_bf16 v[104:107], v[162:165], v[178:181], v[142:145]
	v_mfma_f32_16x16x32_bf16 v[108:111], v[170:173], v[178:181], v[138:141]
	v_mfma_f32_16x16x32_bf16 v[116:119], v[162:165], v[186:189], v[120:123]
	v_mfma_f32_16x16x32_bf16 v[112:115], v[170:173], v[186:189], v[112:115]
	v_mfma_f32_16x16x32_bf16 v[92:95], v[162:165], v[210:213], v[92:95]
	v_mfma_f32_16x16x32_bf16 v[88:91], v[170:173], v[210:213], v[88:91]
	v_mfma_f32_16x16x32_bf16 v[76:79], v[162:165], v[218:221], v[76:79]
	v_mfma_f32_16x16x32_bf16 v[72:75], v[170:173], v[218:221], v[72:75]
	v_mfma_f32_16x16x32_bf16 v[104:107], v[166:169], v[182:185], v[104:107]
	v_mfma_f32_16x16x32_bf16 v[108:111], v[174:177], v[182:185], v[108:111]
	v_mfma_f32_16x16x32_bf16 v[116:119], v[166:169], v[190:193], v[116:119]
	v_mfma_f32_16x16x32_bf16 v[112:115], v[174:177], v[190:193], v[112:115]
	v_mfma_f32_16x16x32_bf16 v[92:95], v[166:169], v[214:217], v[92:95]
	v_mfma_f32_16x16x32_bf16 v[88:91], v[174:177], v[214:217], v[88:91]
	v_mfma_f32_16x16x32_bf16 v[76:79], v[166:169], v[222:225], v[76:79]
	v_mfma_f32_16x16x32_bf16 v[72:75], v[174:177], v[222:225], v[72:75]
	v_mfma_f32_16x16x32_bf16 v[120:123], v[146:149], v[178:181], v[134:137]
	v_mfma_f32_16x16x32_bf16 v[130:133], v[150:153], v[182:185], v[120:123]
	v_mfma_f32_16x16x32_bf16 v[120:123], v[154:157], v[178:181], v[124:127]
	v_mfma_f32_16x16x32_bf16 v[100:103], v[146:149], v[186:189], v[100:103]
	v_mfma_f32_16x16x32_bf16 v[96:99], v[154:157], v[186:189], v[96:99]
	v_mfma_f32_16x16x32_bf16 v[84:87], v[146:149], v[210:213], v[84:87]
	v_mfma_f32_16x16x32_bf16 v[80:83], v[154:157], v[210:213], v[80:83]
	v_mfma_f32_16x16x32_bf16 v[68:71], v[146:149], v[218:221], v[68:71]
	v_mfma_f32_16x16x32_bf16 v[64:67], v[154:157], v[218:221], v[64:67]
	v_mfma_f32_16x16x32_bf16 v[124:127], v[158:161], v[182:185], v[120:123]
	v_mfma_f32_16x16x32_bf16 v[100:103], v[150:153], v[190:193], v[100:103]
	v_mfma_f32_16x16x32_bf16 v[96:99], v[158:161], v[190:193], v[96:99]
	v_mfma_f32_16x16x32_bf16 v[84:87], v[150:153], v[214:217], v[84:87]
	v_mfma_f32_16x16x32_bf16 v[80:83], v[158:161], v[214:217], v[80:83]
	v_mfma_f32_16x16x32_bf16 v[68:71], v[150:153], v[222:225], v[68:71]
	v_mfma_f32_16x16x32_bf16 v[64:67], v[158:161], v[222:225], v[64:67]
	s_barrier
	s_add_i32 s60, vcc_lo, s39
	v_lshl_add_u64 v[210:211], s[84:85], 0, v[198:199]
	s_mov_b32 m0, s60
	ds_read_b128 v[186:189], v236 offset:16384
	ds_read_b128 v[190:193], v236 offset:17408
	ds_read_b128 v[178:181], v236 offset:18432
	ds_read_b128 v[182:185], v236 offset:19456
	ds_read_b128 v[138:141], v236 offset:20480
	ds_read_b128 v[142:145], v236 offset:21504
	ds_read_b128 v[120:123], v236 offset:22528
	ds_read_b128 v[134:137], v236 offset:23552
	global_load_lds_dwordx4 v[210:211], off
	s_add_i32 m0, s60, 0x2000
	s_add_u32 s60, s84, 0x80000
	v_lshl_add_u64 v[212:213], s[84:85], 0, v[200:201]
	s_addc_u32 s61, s85, 0
	s_add_i32 s81, s81, s39
	global_load_lds_dwordx4 v[212:213], off
	s_mov_b32 m0, s81
	v_lshl_add_u64 v[216:217], s[24:25], 0, v[200:201]
	global_load_lds_dwordx4 v198, s[60:61]
	s_add_i32 m0, s81, 0x2000
	v_cndmask_b32_e64 v128, 0, 1, s[96:97]
	global_load_lds_dwordx4 v200, s[60:61]
	v_lshl_add_u64 v[214:215], s[24:25], 0, v[198:199]
	s_mov_b32 m0, s53
	v_cmp_ne_u32_e64 s[60:61], 1, v128
	global_load_lds_dwordx4 v[214:215], off
	s_mov_b32 m0, s88
	s_andn2_b64 vcc, exec, s[96:97]
	global_load_lds_dwordx4 v[216:217], off
	s_waitcnt vmcnt(8) lgkmcnt(0)
	s_barrier
	s_cbranch_vccnz .LBB0_971
	s_waitcnt lgkmcnt(0)
	v_mfma_f32_16x16x32_bf16 v[60:63], v[162:165], v[186:189], v[60:63]
	v_mfma_f32_16x16x32_bf16 v[56:59], v[170:173], v[186:189], v[56:59]
	v_mfma_f32_16x16x32_bf16 v[44:47], v[162:165], v[178:181], v[44:47]
	v_mfma_f32_16x16x32_bf16 v[40:43], v[170:173], v[178:181], v[40:43]
	v_mfma_f32_16x16x32_bf16 v[28:31], v[162:165], v[138:141], v[28:31]
	v_mfma_f32_16x16x32_bf16 v[24:27], v[170:173], v[138:141], v[24:27]
	v_mfma_f32_16x16x32_bf16 v[12:15], v[162:165], v[120:123], v[12:15]
	v_mfma_f32_16x16x32_bf16 v[8:11], v[170:173], v[120:123], v[8:11]
	v_mfma_f32_16x16x32_bf16 v[60:63], v[166:169], v[190:193], v[60:63]
	v_mfma_f32_16x16x32_bf16 v[56:59], v[174:177], v[190:193], v[56:59]
	v_mfma_f32_16x16x32_bf16 v[44:47], v[166:169], v[182:185], v[44:47]
	v_mfma_f32_16x16x32_bf16 v[40:43], v[174:177], v[182:185], v[40:43]
	v_mfma_f32_16x16x32_bf16 v[28:31], v[166:169], v[142:145], v[28:31]
	v_mfma_f32_16x16x32_bf16 v[24:27], v[174:177], v[142:145], v[24:27]
	v_mfma_f32_16x16x32_bf16 v[12:15], v[166:169], v[134:137], v[12:15]
	v_mfma_f32_16x16x32_bf16 v[8:11], v[174:177], v[134:137], v[8:11]
	v_mfma_f32_16x16x32_bf16 v[52:55], v[146:149], v[186:189], v[52:55]
	v_mfma_f32_16x16x32_bf16 v[48:51], v[154:157], v[186:189], v[48:51]
	v_mfma_f32_16x16x32_bf16 v[36:39], v[146:149], v[178:181], v[36:39]
	v_mfma_f32_16x16x32_bf16 v[32:35], v[154:157], v[178:181], v[32:35]
	v_mfma_f32_16x16x32_bf16 v[20:23], v[146:149], v[138:141], v[20:23]
	v_mfma_f32_16x16x32_bf16 v[16:19], v[154:157], v[138:141], v[16:19]
	v_mfma_f32_16x16x32_bf16 v[4:7], v[146:149], v[120:123], v[4:7]
	v_mfma_f32_16x16x32_bf16 v[0:3], v[154:157], v[120:123], v[0:3]
	v_mfma_f32_16x16x32_bf16 v[52:55], v[150:153], v[190:193], v[52:55]
	v_mfma_f32_16x16x32_bf16 v[48:51], v[158:161], v[190:193], v[48:51]
	v_mfma_f32_16x16x32_bf16 v[36:39], v[150:153], v[182:185], v[36:39]
	v_mfma_f32_16x16x32_bf16 v[32:35], v[158:161], v[182:185], v[32:35]
	v_mfma_f32_16x16x32_bf16 v[20:23], v[150:153], v[142:145], v[20:23]
	v_mfma_f32_16x16x32_bf16 v[16:19], v[158:161], v[142:145], v[16:19]
	v_mfma_f32_16x16x32_bf16 v[4:7], v[150:153], v[134:137], v[4:7]
	v_mfma_f32_16x16x32_bf16 v[0:3], v[158:161], v[134:137], v[0:3]
.LBB0_971:
	s_barrier
	s_add_i32 s81, 0, 0x18000
	s_waitcnt lgkmcnt(0)
	v_add_u32_e32 v120, s81, v234
	s_add_i32 vcc_lo, 0, 0x1c000
	ds_read_b128 v[162:165], v120
	ds_read_b128 v[166:169], v120 offset:1024
	ds_read_b128 v[170:173], v120 offset:2048
	ds_read_b128 v[174:177], v120 offset:3072
	v_add_u32_e32 v120, vcc_lo, v234
	ds_read_b128 v[146:149], v120
	ds_read_b128 v[150:153], v120 offset:1024
	ds_read_b128 v[154:157], v120 offset:2048
	ds_read_b128 v[158:161], v120 offset:3072
	s_and_b64 s[26:27], s[26:27], exec
	s_cselect_b32 s27, s72, s20
	s_cselect_b32 s26, 0, s21
	s_add_u32 s24, s24, s27
	s_addc_u32 s25, s25, s26
	s_mov_b32 m0, s89
	ds_read_b128 v[178:181], v236 offset:32768
	ds_read_b128 v[182:185], v236 offset:33792
	ds_read_b128 v[186:189], v236 offset:34816
	ds_read_b128 v[190:193], v236 offset:35840
	ds_read_b128 v[218:221], v236 offset:36864
	ds_read_b128 v[222:225], v236 offset:37888
	ds_read_b128 v[226:229], v236 offset:38912
	ds_read_b128 v[238:241], v236 offset:39936
	global_load_lds_dwordx4 v198, s[24:25]
	s_mov_b32 m0, s90
	v_lshl_add_u64 v[120:121], s[24:25], 0, v[200:201]
	global_load_lds_dwordx4 v[120:121], off
	s_waitcnt vmcnt(8) lgkmcnt(0)
	s_barrier
	v_mfma_f32_16x16x32_bf16 v[104:107], v[162:165], v[178:181], v[104:107]
	v_mfma_f32_16x16x32_bf16 v[142:145], v[166:169], v[182:185], v[104:107]
	v_mfma_f32_16x16x32_bf16 v[104:107], v[170:173], v[178:181], v[108:111]
	v_mfma_f32_16x16x32_bf16 v[138:141], v[174:177], v[182:185], v[104:107]
	v_mfma_f32_16x16x32_bf16 v[104:107], v[162:165], v[186:189], v[116:119]
	v_mfma_f32_16x16x32_bf16 v[120:123], v[166:169], v[190:193], v[104:107]
	v_mfma_f32_16x16x32_bf16 v[104:107], v[170:173], v[186:189], v[112:115]
	v_mfma_f32_16x16x32_bf16 v[92:95], v[162:165], v[218:221], v[92:95]
	v_mfma_f32_16x16x32_bf16 v[88:91], v[170:173], v[218:221], v[88:91]
	v_mfma_f32_16x16x32_bf16 v[76:79], v[162:165], v[226:229], v[76:79]
	v_mfma_f32_16x16x32_bf16 v[72:75], v[170:173], v[226:229], v[72:75]
	v_mfma_f32_16x16x32_bf16 v[112:115], v[174:177], v[190:193], v[104:107]
	v_mfma_f32_16x16x32_bf16 v[92:95], v[166:169], v[222:225], v[92:95]
	v_mfma_f32_16x16x32_bf16 v[88:91], v[174:177], v[222:225], v[88:91]
	v_mfma_f32_16x16x32_bf16 v[76:79], v[166:169], v[238:241], v[76:79]
	v_mfma_f32_16x16x32_bf16 v[72:75], v[174:177], v[238:241], v[72:75]
	v_mfma_f32_16x16x32_bf16 v[104:107], v[146:149], v[178:181], v[130:133]
	v_mfma_f32_16x16x32_bf16 v[134:137], v[150:153], v[182:185], v[104:107]
	v_mfma_f32_16x16x32_bf16 v[104:107], v[154:157], v[178:181], v[124:127]
	v_mfma_f32_16x16x32_bf16 v[100:103], v[146:149], v[186:189], v[100:103]
	v_mfma_f32_16x16x32_bf16 v[96:99], v[154:157], v[186:189], v[96:99]
	v_mfma_f32_16x16x32_bf16 v[84:87], v[146:149], v[218:221], v[84:87]
	v_mfma_f32_16x16x32_bf16 v[80:83], v[154:157], v[218:221], v[80:83]
	v_mfma_f32_16x16x32_bf16 v[68:71], v[146:149], v[226:229], v[68:71]
	v_mfma_f32_16x16x32_bf16 v[64:67], v[154:157], v[226:229], v[64:67]
	v_mfma_f32_16x16x32_bf16 v[124:127], v[158:161], v[182:185], v[104:107]
	v_mfma_f32_16x16x32_bf16 v[100:103], v[150:153], v[190:193], v[100:103]
	v_mfma_f32_16x16x32_bf16 v[96:99], v[158:161], v[190:193], v[96:99]
	v_mfma_f32_16x16x32_bf16 v[84:87], v[150:153], v[222:225], v[84:87]
	v_mfma_f32_16x16x32_bf16 v[80:83], v[158:161], v[222:225], v[80:83]
	v_mfma_f32_16x16x32_bf16 v[68:71], v[150:153], v[238:241], v[68:71]
	v_mfma_f32_16x16x32_bf16 v[64:67], v[158:161], v[238:241], v[64:67]
	s_barrier
	s_add_i32 s24, s81, s39
	v_lshl_add_u64 v[210:211], v[210:211], 0, s[42:43]
	s_mov_b32 m0, s24
	ds_read_b128 v[186:189], v236 offset:49152
	ds_read_b128 v[190:193], v236 offset:50176
	ds_read_b128 v[178:181], v236 offset:51200
	ds_read_b128 v[182:185], v236 offset:52224
	ds_read_b128 v[116:119], v236 offset:53248
	ds_read_b128 v[130:133], v236 offset:54272
	ds_read_b128 v[104:107], v236 offset:55296
	ds_read_b128 v[108:111], v236 offset:56320
	global_load_lds_dwordx4 v[210:211], off
	s_add_i32 m0, s24, 0x2000
	s_add_u32 s24, s84, 0x80080
	v_lshl_add_u64 v[210:211], v[212:213], 0, s[42:43]
	s_addc_u32 s25, s85, 0
	s_add_i32 s26, vcc_lo, s39
	global_load_lds_dwordx4 v[210:211], off
	s_mov_b32 m0, s26
	s_and_b64 vcc, exec, s[60:61]
	global_load_lds_dwordx4 v198, s[24:25]
	s_add_i32 m0, s26, 0x2000
	s_nop 0
	global_load_lds_dwordx4 v200, s[24:25]
	s_mov_b32 m0, s94
	v_lshl_add_u64 v[210:211], v[214:215], 0, s[42:43]
	global_load_lds_dwordx4 v[210:211], off
	s_mov_b32 m0, s33
	v_lshl_add_u64 v[210:211], v[216:217], 0, s[42:43]
	global_load_lds_dwordx4 v[210:211], off
	s_waitcnt vmcnt(8) lgkmcnt(0)
	s_barrier
	s_cbranch_vccnz .LBB0_968
	s_waitcnt lgkmcnt(0)
	v_mfma_f32_16x16x32_bf16 v[60:63], v[162:165], v[186:189], v[60:63]
	v_mfma_f32_16x16x32_bf16 v[56:59], v[170:173], v[186:189], v[56:59]
	v_mfma_f32_16x16x32_bf16 v[44:47], v[162:165], v[178:181], v[44:47]
	v_mfma_f32_16x16x32_bf16 v[40:43], v[170:173], v[178:181], v[40:43]
	v_mfma_f32_16x16x32_bf16 v[28:31], v[162:165], v[116:119], v[28:31]
	v_mfma_f32_16x16x32_bf16 v[24:27], v[170:173], v[116:119], v[24:27]
	v_mfma_f32_16x16x32_bf16 v[12:15], v[162:165], v[104:107], v[12:15]
	v_mfma_f32_16x16x32_bf16 v[8:11], v[170:173], v[104:107], v[8:11]
	v_mfma_f32_16x16x32_bf16 v[60:63], v[166:169], v[190:193], v[60:63]
	v_mfma_f32_16x16x32_bf16 v[56:59], v[174:177], v[190:193], v[56:59]
	v_mfma_f32_16x16x32_bf16 v[44:47], v[166:169], v[182:185], v[44:47]
	v_mfma_f32_16x16x32_bf16 v[40:43], v[174:177], v[182:185], v[40:43]
	v_mfma_f32_16x16x32_bf16 v[28:31], v[166:169], v[130:133], v[28:31]
	v_mfma_f32_16x16x32_bf16 v[24:27], v[174:177], v[130:133], v[24:27]
	v_mfma_f32_16x16x32_bf16 v[12:15], v[166:169], v[108:111], v[12:15]
	v_mfma_f32_16x16x32_bf16 v[8:11], v[174:177], v[108:111], v[8:11]
	v_mfma_f32_16x16x32_bf16 v[52:55], v[146:149], v[186:189], v[52:55]
	v_mfma_f32_16x16x32_bf16 v[48:51], v[154:157], v[186:189], v[48:51]
	v_mfma_f32_16x16x32_bf16 v[36:39], v[146:149], v[178:181], v[36:39]
	v_mfma_f32_16x16x32_bf16 v[32:35], v[154:157], v[178:181], v[32:35]
	v_mfma_f32_16x16x32_bf16 v[20:23], v[146:149], v[116:119], v[20:23]
	v_mfma_f32_16x16x32_bf16 v[16:19], v[154:157], v[116:119], v[16:19]
	v_mfma_f32_16x16x32_bf16 v[4:7], v[146:149], v[104:107], v[4:7]
	v_mfma_f32_16x16x32_bf16 v[0:3], v[154:157], v[104:107], v[0:3]
	v_mfma_f32_16x16x32_bf16 v[52:55], v[150:153], v[190:193], v[52:55]
	v_mfma_f32_16x16x32_bf16 v[48:51], v[158:161], v[190:193], v[48:51]
	v_mfma_f32_16x16x32_bf16 v[36:39], v[150:153], v[182:185], v[36:39]
	v_mfma_f32_16x16x32_bf16 v[32:35], v[158:161], v[182:185], v[32:35]
	v_mfma_f32_16x16x32_bf16 v[20:23], v[150:153], v[130:133], v[20:23]
	v_mfma_f32_16x16x32_bf16 v[16:19], v[158:161], v[130:133], v[16:19]
	v_mfma_f32_16x16x32_bf16 v[4:7], v[150:153], v[108:111], v[4:7]
	v_mfma_f32_16x16x32_bf16 v[0:3], v[158:161], v[108:111], v[0:3]
	s_branch .LBB0_968

.LBB0_1400:
	s_add_u32 s2, s64, s74
	s_addc_u32 s3, s65, s75
	s_add_u32 s22, s2, 0x28c00100
	s_addc_u32 s23, s3, 0
	s_cmpk_eq_i32 s74, 0xf00
	s_cselect_b64 s[60:61], -1, 0
	s_and_b64 s[2:3], s[60:61], exec
	s_cselect_b32 s23, s9, s23
	s_cselect_b32 s22, s8, s22
	v_add_u32_e32 v128, s26, v242
	s_add_i32 s2, 0, 0x14000
	v_lshl_add_u64 v[146:147], v[220:221], 0, s[74:75]
	ds_read_b128 v[130:133], v128
	ds_read_b128 v[134:137], v128 offset:1024
	ds_read_b128 v[138:141], v128 offset:2048
	ds_read_b128 v[142:145], v128 offset:3072
	v_add_u32_e32 v128, s2, v242
	v_cndmask_b32_e64 v223, v147, v207, s[60:61]
	v_cndmask_b32_e64 v222, v146, v206, s[60:61]
	ds_read_b128 v[146:149], v128
	ds_read_b128 v[150:153], v128 offset:1024
	ds_read_b128 v[154:157], v128 offset:2048
	ds_read_b128 v[158:161], v128 offset:3072
	v_lshl_add_u64 v[194:195], v[218:219], 0, s[74:75]
	s_add_i32 m0, s36, 0xc000
	ds_read_b128 v[162:165], v209
	ds_read_b128 v[166:169], v209 offset:1024
	ds_read_b128 v[170:173], v209 offset:2048
	ds_read_b128 v[174:177], v209 offset:3072
	ds_read_b128 v[178:181], v209 offset:4096
	ds_read_b128 v[182:185], v209 offset:5120
	ds_read_b128 v[186:189], v209 offset:6144
	ds_read_b128 v[190:193], v209 offset:7168
	global_load_lds_dwordx4 v[194:195], off
	s_add_i32 m0, s36, 0xe000
	v_lshl_add_u64 v[194:195], v[216:217], 0, s[74:75]
	global_load_lds_dwordx4 v[194:195], off
	s_waitcnt vmcnt(8) lgkmcnt(0)
	s_barrier
	v_mfma_f32_16x16x32_bf16 v[124:127], v[130:133], v[162:165], v[124:127]
	v_mfma_f32_16x16x32_bf16 v[120:123], v[138:141], v[162:165], v[120:123]
	v_mfma_f32_16x16x32_bf16 v[108:111], v[130:133], v[170:173], v[108:111]
	v_mfma_f32_16x16x32_bf16 v[104:107], v[138:141], v[170:173], v[104:107]
	v_mfma_f32_16x16x32_bf16 v[92:95], v[130:133], v[178:181], v[92:95]
	v_mfma_f32_16x16x32_bf16 v[88:91], v[138:141], v[178:181], v[88:91]
	v_mfma_f32_16x16x32_bf16 v[76:79], v[130:133], v[186:189], v[76:79]
	v_mfma_f32_16x16x32_bf16 v[72:75], v[138:141], v[186:189], v[72:75]
	v_mfma_f32_16x16x32_bf16 v[124:127], v[134:137], v[166:169], v[124:127]
	v_mfma_f32_16x16x32_bf16 v[120:123], v[142:145], v[166:169], v[120:123]
	v_mfma_f32_16x16x32_bf16 v[108:111], v[134:137], v[174:177], v[108:111]
	v_mfma_f32_16x16x32_bf16 v[104:107], v[142:145], v[174:177], v[104:107]
	v_mfma_f32_16x16x32_bf16 v[92:95], v[134:137], v[182:185], v[92:95]
	v_mfma_f32_16x16x32_bf16 v[88:91], v[142:145], v[182:185], v[88:91]
	v_mfma_f32_16x16x32_bf16 v[76:79], v[134:137], v[190:193], v[76:79]
	v_mfma_f32_16x16x32_bf16 v[72:75], v[142:145], v[190:193], v[72:75]
	v_mfma_f32_16x16x32_bf16 v[116:119], v[146:149], v[162:165], v[116:119]
	v_mfma_f32_16x16x32_bf16 v[112:115], v[154:157], v[162:165], v[112:115]
	v_mfma_f32_16x16x32_bf16 v[100:103], v[146:149], v[170:173], v[100:103]
	v_mfma_f32_16x16x32_bf16 v[96:99], v[154:157], v[170:173], v[96:99]
	v_mfma_f32_16x16x32_bf16 v[84:87], v[146:149], v[178:181], v[84:87]
	v_mfma_f32_16x16x32_bf16 v[80:83], v[154:157], v[178:181], v[80:83]
	v_mfma_f32_16x16x32_bf16 v[68:71], v[146:149], v[186:189], v[68:71]
	v_mfma_f32_16x16x32_bf16 v[64:67], v[154:157], v[186:189], v[64:67]
	v_mfma_f32_16x16x32_bf16 v[116:119], v[150:153], v[166:169], v[116:119]
	v_mfma_f32_16x16x32_bf16 v[112:115], v[158:161], v[166:169], v[112:115]
	v_mfma_f32_16x16x32_bf16 v[100:103], v[150:153], v[174:177], v[100:103]
	v_mfma_f32_16x16x32_bf16 v[96:99], v[158:161], v[174:177], v[96:99]
	v_mfma_f32_16x16x32_bf16 v[84:87], v[150:153], v[182:185], v[84:87]
	v_mfma_f32_16x16x32_bf16 v[80:83], v[158:161], v[182:185], v[80:83]
	v_mfma_f32_16x16x32_bf16 v[68:71], v[150:153], v[190:193], v[68:71]
	v_mfma_f32_16x16x32_bf16 v[64:67], v[158:161], v[190:193], v[64:67]
	s_barrier
	s_add_i32 s3, s26, s33
	v_lshl_add_u64 v[224:225], v[222:223], 0, v[198:199]
	s_mov_b32 m0, s3
	ds_read_b128 v[186:189], v209 offset:16384
	ds_read_b128 v[190:193], v209 offset:17408
	ds_read_b128 v[178:181], v209 offset:18432
	ds_read_b128 v[182:185], v209 offset:19456
	ds_read_b128 v[170:173], v209 offset:20480
	ds_read_b128 v[174:177], v209 offset:21504
	ds_read_b128 v[162:165], v209 offset:22528
	ds_read_b128 v[166:169], v209 offset:23552
	global_load_lds_dwordx4 v[224:225], off
	v_lshl_add_u64 v[226:227], v[222:223], 0, v[200:201]
	s_add_i32 m0, s3, 0x2000
	v_lshl_add_u64 v[194:195], v[222:223], 0, s[40:41]
	s_add_i32 s2, s2, s33
	global_load_lds_dwordx4 v[226:227], off
	v_lshl_add_u64 v[196:197], v[194:195], 0, v[198:199]
	s_mov_b32 m0, s2
	v_lshl_add_u64 v[194:195], v[194:195], 0, v[200:201]
	global_load_lds_dwordx4 v[196:197], off
	s_add_i32 m0, s2, 0x2000
	v_cndmask_b32_e64 v128, v208, v211, s[60:61]
	global_load_lds_dwordx4 v[194:195], off
	s_mov_b32 m0, s36
	v_cndmask_b32_e64 v228, v210, v243, s[60:61]
	global_load_lds_dwordx4 v128, s[22:23]
	s_mov_b32 m0, s37
	v_cndmask_b32_e64 v194, 0, 1, s[20:21]
	global_load_lds_dwordx4 v228, s[22:23]
	s_waitcnt vmcnt(8) lgkmcnt(0)
	v_cmp_ne_u32_e64 s[62:63], 1, v194
	s_andn2_b64 vcc, exec, s[20:21]
	s_barrier
	s_cbranch_vccnz .LBB0_1402
	s_waitcnt lgkmcnt(0)
	v_mfma_f32_16x16x32_bf16 v[60:63], v[130:133], v[186:189], v[60:63]
	v_mfma_f32_16x16x32_bf16 v[56:59], v[138:141], v[186:189], v[56:59]
	v_mfma_f32_16x16x32_bf16 v[44:47], v[130:133], v[178:181], v[44:47]
	v_mfma_f32_16x16x32_bf16 v[40:43], v[138:141], v[178:181], v[40:43]
	v_mfma_f32_16x16x32_bf16 v[28:31], v[130:133], v[170:173], v[28:31]
	v_mfma_f32_16x16x32_bf16 v[24:27], v[138:141], v[170:173], v[24:27]
	v_mfma_f32_16x16x32_bf16 v[12:15], v[130:133], v[162:165], v[12:15]
	v_mfma_f32_16x16x32_bf16 v[8:11], v[138:141], v[162:165], v[8:11]
	v_mfma_f32_16x16x32_bf16 v[60:63], v[134:137], v[190:193], v[60:63]
	v_mfma_f32_16x16x32_bf16 v[56:59], v[142:145], v[190:193], v[56:59]
	v_mfma_f32_16x16x32_bf16 v[44:47], v[134:137], v[182:185], v[44:47]
	v_mfma_f32_16x16x32_bf16 v[40:43], v[142:145], v[182:185], v[40:43]
	v_mfma_f32_16x16x32_bf16 v[28:31], v[134:137], v[174:177], v[28:31]
	v_mfma_f32_16x16x32_bf16 v[24:27], v[142:145], v[174:177], v[24:27]
	v_mfma_f32_16x16x32_bf16 v[12:15], v[134:137], v[166:169], v[12:15]
	v_mfma_f32_16x16x32_bf16 v[8:11], v[142:145], v[166:169], v[8:11]
	v_mfma_f32_16x16x32_bf16 v[52:55], v[146:149], v[186:189], v[52:55]
	v_mfma_f32_16x16x32_bf16 v[48:51], v[154:157], v[186:189], v[48:51]
	v_mfma_f32_16x16x32_bf16 v[36:39], v[146:149], v[178:181], v[36:39]
	v_mfma_f32_16x16x32_bf16 v[32:35], v[154:157], v[178:181], v[32:35]
	v_mfma_f32_16x16x32_bf16 v[20:23], v[146:149], v[170:173], v[20:23]
	v_mfma_f32_16x16x32_bf16 v[16:19], v[154:157], v[170:173], v[16:19]
	v_mfma_f32_16x16x32_bf16 v[4:7], v[146:149], v[162:165], v[4:7]
	v_mfma_f32_16x16x32_bf16 v[0:3], v[154:157], v[162:165], v[0:3]
	v_mfma_f32_16x16x32_bf16 v[52:55], v[150:153], v[190:193], v[52:55]
	v_mfma_f32_16x16x32_bf16 v[48:51], v[158:161], v[190:193], v[48:51]
	v_mfma_f32_16x16x32_bf16 v[36:39], v[150:153], v[182:185], v[36:39]
	v_mfma_f32_16x16x32_bf16 v[32:35], v[158:161], v[182:185], v[32:35]
	v_mfma_f32_16x16x32_bf16 v[20:23], v[150:153], v[174:177], v[20:23]
	v_mfma_f32_16x16x32_bf16 v[16:19], v[158:161], v[174:177], v[16:19]
	v_mfma_f32_16x16x32_bf16 v[4:7], v[150:153], v[166:169], v[4:7]
	v_mfma_f32_16x16x32_bf16 v[0:3], v[158:161], v[166:169], v[0:3]
.LBB0_1402:
	v_mov_b32_e32 v229, v129
	v_lshl_add_u64 v[194:195], s[22:23], 0, v[128:129]
	v_lshl_add_u64 v[196:197], s[22:23], 0, v[228:229]
	s_barrier
	s_add_i32 s2, 0, 0x18000
	v_add_u32_e32 v128, s2, v242
	s_add_i32 s3, 0, 0x1c000
	ds_read_b128 v[146:149], v128
	ds_read_b128 v[150:153], v128 offset:1024
	ds_read_b128 v[154:157], v128 offset:2048
	ds_read_b128 v[158:161], v128 offset:3072
	v_add_u32_e32 v128, s3, v242
	ds_read_b128 v[130:133], v128
	ds_read_b128 v[134:137], v128 offset:1024
	ds_read_b128 v[138:141], v128 offset:2048
	ds_read_b128 v[142:145], v128 offset:3072
	s_mov_b32 m0, s38
	v_cndmask_b32_e64 v128, v212, v244, s[60:61]
	ds_read_b128 v[162:165], v209 offset:32768
	ds_read_b128 v[166:169], v209 offset:33792
	ds_read_b128 v[170:173], v209 offset:34816
	ds_read_b128 v[174:177], v209 offset:35840
	ds_read_b128 v[178:181], v209 offset:36864
	ds_read_b128 v[182:185], v209 offset:37888
	ds_read_b128 v[186:189], v209 offset:38912
	ds_read_b128 v[190:193], v209 offset:39936
	global_load_lds_dwordx4 v128, s[22:23]
	v_cndmask_b32_e64 v128, v214, v245, s[60:61]
	s_mov_b32 m0, s39
	s_nop 0
	global_load_lds_dwordx4 v128, s[22:23]
	s_waitcnt vmcnt(8) lgkmcnt(0)
	s_barrier
	v_mfma_f32_16x16x32_bf16 v[124:127], v[146:149], v[162:165], v[124:127]
	v_mfma_f32_16x16x32_bf16 v[120:123], v[154:157], v[162:165], v[120:123]
	v_mfma_f32_16x16x32_bf16 v[108:111], v[146:149], v[170:173], v[108:111]
	v_mfma_f32_16x16x32_bf16 v[104:107], v[154:157], v[170:173], v[104:107]
	v_mfma_f32_16x16x32_bf16 v[92:95], v[146:149], v[178:181], v[92:95]
	v_mfma_f32_16x16x32_bf16 v[88:91], v[154:157], v[178:181], v[88:91]
	v_mfma_f32_16x16x32_bf16 v[76:79], v[146:149], v[186:189], v[76:79]
	v_mfma_f32_16x16x32_bf16 v[72:75], v[154:157], v[186:189], v[72:75]
	v_mfma_f32_16x16x32_bf16 v[124:127], v[150:153], v[166:169], v[124:127]
	v_mfma_f32_16x16x32_bf16 v[120:123], v[158:161], v[166:169], v[120:123]
	v_mfma_f32_16x16x32_bf16 v[108:111], v[150:153], v[174:177], v[108:111]
	v_mfma_f32_16x16x32_bf16 v[104:107], v[158:161], v[174:177], v[104:107]
	v_mfma_f32_16x16x32_bf16 v[92:95], v[150:153], v[182:185], v[92:95]
	v_mfma_f32_16x16x32_bf16 v[88:91], v[158:161], v[182:185], v[88:91]
	v_mfma_f32_16x16x32_bf16 v[76:79], v[150:153], v[190:193], v[76:79]
	v_mfma_f32_16x16x32_bf16 v[72:75], v[158:161], v[190:193], v[72:75]
	v_mfma_f32_16x16x32_bf16 v[116:119], v[130:133], v[162:165], v[116:119]
	v_mfma_f32_16x16x32_bf16 v[112:115], v[138:141], v[162:165], v[112:115]
	v_mfma_f32_16x16x32_bf16 v[100:103], v[130:133], v[170:173], v[100:103]
	v_mfma_f32_16x16x32_bf16 v[96:99], v[138:141], v[170:173], v[96:99]
	v_mfma_f32_16x16x32_bf16 v[84:87], v[130:133], v[178:181], v[84:87]
	v_mfma_f32_16x16x32_bf16 v[80:83], v[138:141], v[178:181], v[80:83]
	v_mfma_f32_16x16x32_bf16 v[68:71], v[130:133], v[186:189], v[68:71]
	v_mfma_f32_16x16x32_bf16 v[64:67], v[138:141], v[186:189], v[64:67]
	v_mfma_f32_16x16x32_bf16 v[116:119], v[134:137], v[166:169], v[116:119]
	v_mfma_f32_16x16x32_bf16 v[112:115], v[142:145], v[166:169], v[112:115]
	v_mfma_f32_16x16x32_bf16 v[100:103], v[134:137], v[174:177], v[100:103]
	v_mfma_f32_16x16x32_bf16 v[96:99], v[142:145], v[174:177], v[96:99]
	v_mfma_f32_16x16x32_bf16 v[84:87], v[134:137], v[182:185], v[84:87]
	v_mfma_f32_16x16x32_bf16 v[80:83], v[142:145], v[182:185], v[80:83]
	v_mfma_f32_16x16x32_bf16 v[68:71], v[134:137], v[190:193], v[68:71]
	v_mfma_f32_16x16x32_bf16 v[64:67], v[142:145], v[190:193], v[64:67]
	s_barrier
	s_add_i32 s2, s2, s33
	v_lshl_add_u64 v[224:225], v[224:225], 0, s[42:43]
	s_mov_b32 m0, s2
	ds_read_b128 v[186:189], v209 offset:49152
	ds_read_b128 v[190:193], v209 offset:50176
	ds_read_b128 v[178:181], v209 offset:51200
	ds_read_b128 v[182:185], v209 offset:52224
	ds_read_b128 v[170:173], v209 offset:53248
	ds_read_b128 v[174:177], v209 offset:54272
	ds_read_b128 v[162:165], v209 offset:55296
	ds_read_b128 v[166:169], v209 offset:56320
	global_load_lds_dwordx4 v[224:225], off
	v_lshl_add_u64 v[224:225], v[226:227], 0, s[42:43]
	s_add_i32 m0, s2, 0x2000
	v_lshl_add_u64 v[222:223], v[222:223], 0, s[44:45]
	s_add_i32 s2, s3, s33
	global_load_lds_dwordx4 v[224:225], off
	v_lshl_add_u64 v[224:225], v[222:223], 0, v[198:199]
	s_mov_b32 m0, s2
	v_lshl_add_u64 v[222:223], v[222:223], 0, v[200:201]
	global_load_lds_dwordx4 v[224:225], off
	s_add_i32 m0, s2, 0x2000
	v_lshl_add_u64 v[194:195], v[194:195], 0, s[42:43]
	global_load_lds_dwordx4 v[222:223], off
	s_mov_b32 m0, s76
	s_and_b64 vcc, exec, s[62:63]
	global_load_lds_dwordx4 v[194:195], off
	s_mov_b32 m0, s77
	v_lshl_add_u64 v[194:195], v[196:197], 0, s[42:43]
	global_load_lds_dwordx4 v[194:195], off
	s_waitcnt vmcnt(8) lgkmcnt(0)
	s_barrier
	s_cbranch_vccnz .LBB0_1399
	s_waitcnt lgkmcnt(0)
	v_mfma_f32_16x16x32_bf16 v[60:63], v[146:149], v[186:189], v[60:63]
	v_mfma_f32_16x16x32_bf16 v[56:59], v[154:157], v[186:189], v[56:59]
	v_mfma_f32_16x16x32_bf16 v[44:47], v[146:149], v[178:181], v[44:47]
	v_mfma_f32_16x16x32_bf16 v[40:43], v[154:157], v[178:181], v[40:43]
	v_mfma_f32_16x16x32_bf16 v[28:31], v[146:149], v[170:173], v[28:31]
	v_mfma_f32_16x16x32_bf16 v[24:27], v[154:157], v[170:173], v[24:27]
	v_mfma_f32_16x16x32_bf16 v[12:15], v[146:149], v[162:165], v[12:15]
	v_mfma_f32_16x16x32_bf16 v[8:11], v[154:157], v[162:165], v[8:11]
	v_mfma_f32_16x16x32_bf16 v[60:63], v[150:153], v[190:193], v[60:63]
	v_mfma_f32_16x16x32_bf16 v[56:59], v[158:161], v[190:193], v[56:59]
	v_mfma_f32_16x16x32_bf16 v[44:47], v[150:153], v[182:185], v[44:47]
	v_mfma_f32_16x16x32_bf16 v[40:43], v[158:161], v[182:185], v[40:43]
	v_mfma_f32_16x16x32_bf16 v[28:31], v[150:153], v[174:177], v[28:31]
	v_mfma_f32_16x16x32_bf16 v[24:27], v[158:161], v[174:177], v[24:27]
	v_mfma_f32_16x16x32_bf16 v[12:15], v[150:153], v[166:169], v[12:15]
	v_mfma_f32_16x16x32_bf16 v[8:11], v[158:161], v[166:169], v[8:11]
	v_mfma_f32_16x16x32_bf16 v[52:55], v[130:133], v[186:189], v[52:55]
	v_mfma_f32_16x16x32_bf16 v[48:51], v[138:141], v[186:189], v[48:51]
	v_mfma_f32_16x16x32_bf16 v[36:39], v[130:133], v[178:181], v[36:39]
	v_mfma_f32_16x16x32_bf16 v[32:35], v[138:141], v[178:181], v[32:35]
	v_mfma_f32_16x16x32_bf16 v[20:23], v[130:133], v[170:173], v[20:23]
	v_mfma_f32_16x16x32_bf16 v[16:19], v[138:141], v[170:173], v[16:19]
	v_mfma_f32_16x16x32_bf16 v[4:7], v[130:133], v[162:165], v[4:7]
	v_mfma_f32_16x16x32_bf16 v[0:3], v[138:141], v[162:165], v[0:3]
	v_mfma_f32_16x16x32_bf16 v[52:55], v[134:137], v[190:193], v[52:55]
	v_mfma_f32_16x16x32_bf16 v[48:51], v[142:145], v[190:193], v[48:51]
	v_mfma_f32_16x16x32_bf16 v[36:39], v[134:137], v[182:185], v[36:39]
	v_mfma_f32_16x16x32_bf16 v[32:35], v[142:145], v[182:185], v[32:35]
	v_mfma_f32_16x16x32_bf16 v[20:23], v[134:137], v[174:177], v[20:23]
	v_mfma_f32_16x16x32_bf16 v[16:19], v[142:145], v[174:177], v[16:19]
	v_mfma_f32_16x16x32_bf16 v[4:7], v[134:137], v[166:169], v[4:7]
	v_mfma_f32_16x16x32_bf16 v[0:3], v[142:145], v[166:169], v[0:3]
	s_branch .LBB0_1399

.LBB0_1443:
	s_lshl_b32 s72, s19, 7
	s_add_u32 s29, s76, s72
	s_addc_u32 s30, s77, 0
	s_add_u32 s22, s29, 0x100
	s_addc_u32 s23, s30, 0
	v_lshl_add_u64 v[144:145], v[142:143], 0, s[72:73]
	s_and_b64 s[2:3], s[60:61], exec
	v_lshl_add_u64 v[144:145], v[144:145], 0, s[46:47]
	s_cselect_b32 s23, s67, s23
	s_cselect_b32 s22, s66, s22
	v_cndmask_b32_e64 v145, v145, v141, s[60:61]
	v_cndmask_b32_e64 v144, v144, v140, s[60:61]
	s_add_i32 s60, 0, 0x10000
	v_add_u32_e32 v128, s60, v147
	s_add_i32 s61, 0, 0x14000
	ds_read_b128 v[150:153], v128
	ds_read_b128 v[154:157], v128 offset:1024
	ds_read_b128 v[158:161], v128 offset:2048
	ds_read_b128 v[162:165], v128 offset:3072
	v_add_u32_e32 v128, s61, v147
	ds_read_b128 v[166:169], v128
	ds_read_b128 v[170:173], v128 offset:1024
	ds_read_b128 v[174:177], v128 offset:2048
	ds_read_b128 v[178:181], v128 offset:3072
	s_add_u32 s2, s29, 0x20080
	s_addc_u32 s3, s30, 0
	s_add_i32 m0, s35, 0xc000
	ds_read_b128 v[182:185], v148
	ds_read_b128 v[186:189], v148 offset:1024
	ds_read_b128 v[190:193], v148 offset:2048
	ds_read_b128 v[198:201], v148 offset:3072
	ds_read_b128 v[202:205], v148 offset:4096
	ds_read_b128 v[206:209], v148 offset:5120
	ds_read_b128 v[210:213], v148 offset:6144
	ds_read_b128 v[214:217], v148 offset:7168
	global_load_lds_dwordx4 v130, s[2:3]
	s_add_i32 m0, s35, 0xe000
	s_nop 0
	global_load_lds_dwordx4 v134, s[2:3]
	s_waitcnt vmcnt(8) lgkmcnt(0)
	s_barrier
	v_mfma_f32_16x16x32_bf16 v[124:127], v[150:153], v[182:185], v[124:127]
	v_mfma_f32_16x16x32_bf16 v[120:123], v[158:161], v[182:185], v[120:123]
	v_mfma_f32_16x16x32_bf16 v[112:115], v[150:153], v[190:193], v[112:115]
	v_mfma_f32_16x16x32_bf16 v[104:107], v[158:161], v[190:193], v[104:107]
	v_mfma_f32_16x16x32_bf16 v[96:99], v[150:153], v[202:205], v[96:99]
	v_mfma_f32_16x16x32_bf16 v[88:91], v[158:161], v[202:205], v[88:91]
	v_mfma_f32_16x16x32_bf16 v[80:83], v[150:153], v[210:213], v[80:83]
	v_mfma_f32_16x16x32_bf16 v[72:75], v[158:161], v[210:213], v[72:75]
	v_mfma_f32_16x16x32_bf16 v[124:127], v[154:157], v[186:189], v[124:127]
	v_mfma_f32_16x16x32_bf16 v[120:123], v[162:165], v[186:189], v[120:123]
	v_mfma_f32_16x16x32_bf16 v[112:115], v[154:157], v[198:201], v[112:115]
	v_mfma_f32_16x16x32_bf16 v[104:107], v[162:165], v[198:201], v[104:107]
	v_mfma_f32_16x16x32_bf16 v[96:99], v[154:157], v[206:209], v[96:99]
	v_mfma_f32_16x16x32_bf16 v[88:91], v[162:165], v[206:209], v[88:91]
	v_mfma_f32_16x16x32_bf16 v[80:83], v[154:157], v[214:217], v[80:83]
	v_mfma_f32_16x16x32_bf16 v[72:75], v[162:165], v[214:217], v[72:75]
	v_mfma_f32_16x16x32_bf16 v[116:119], v[166:169], v[182:185], v[116:119]
	v_mfma_f32_16x16x32_bf16 v[108:111], v[174:177], v[182:185], v[108:111]
	v_mfma_f32_16x16x32_bf16 v[100:103], v[166:169], v[190:193], v[100:103]
	v_mfma_f32_16x16x32_bf16 v[92:95], v[174:177], v[190:193], v[92:95]
	v_mfma_f32_16x16x32_bf16 v[84:87], v[166:169], v[202:205], v[84:87]
	v_mfma_f32_16x16x32_bf16 v[76:79], v[174:177], v[202:205], v[76:79]
	v_mfma_f32_16x16x32_bf16 v[68:71], v[166:169], v[210:213], v[68:71]
	v_mfma_f32_16x16x32_bf16 v[64:67], v[174:177], v[210:213], v[64:67]
	v_mfma_f32_16x16x32_bf16 v[116:119], v[170:173], v[186:189], v[116:119]
	v_mfma_f32_16x16x32_bf16 v[108:111], v[178:181], v[186:189], v[108:111]
	v_mfma_f32_16x16x32_bf16 v[100:103], v[170:173], v[198:201], v[100:103]
	v_mfma_f32_16x16x32_bf16 v[92:95], v[178:181], v[198:201], v[92:95]
	v_mfma_f32_16x16x32_bf16 v[84:87], v[170:173], v[206:209], v[84:87]
	v_mfma_f32_16x16x32_bf16 v[76:79], v[178:181], v[206:209], v[76:79]
	v_mfma_f32_16x16x32_bf16 v[68:71], v[170:173], v[214:217], v[68:71]
	v_mfma_f32_16x16x32_bf16 v[64:67], v[178:181], v[214:217], v[64:67]
	s_barrier
	s_add_i32 s2, s60, s33
	v_lshl_add_u64 v[194:195], v[144:145], 0, v[132:133]
	s_mov_b32 m0, s2
	ds_read_b128 v[182:185], v148 offset:16384
	ds_read_b128 v[186:189], v148 offset:17408
	ds_read_b128 v[190:193], v148 offset:18432
	ds_read_b128 v[198:201], v148 offset:19456
	ds_read_b128 v[202:205], v148 offset:20480
	ds_read_b128 v[206:209], v148 offset:21504
	ds_read_b128 v[210:213], v148 offset:22528
	ds_read_b128 v[214:217], v148 offset:23552
	global_load_lds_dwordx4 v[194:195], off
	v_lshl_add_u64 v[196:197], v[144:145], 0, v[136:137]
	s_add_i32 m0, s2, 0x2000
	v_lshl_add_u64 v[218:219], v[144:145], 0, s[48:49]
	s_add_i32 s2, s61, s33
	global_load_lds_dwordx4 v[196:197], off
	v_lshl_add_u64 v[220:221], v[218:219], 0, v[132:133]
	s_mov_b32 m0, s2
	v_lshl_add_u64 v[218:219], v[218:219], 0, v[136:137]
	global_load_lds_dwordx4 v[220:221], off
	s_add_i32 m0, s2, 0x2000
	v_lshl_add_u64 v[220:221], s[22:23], 0, v[134:135]
	global_load_lds_dwordx4 v[218:219], off
	s_mov_b32 m0, s35
	v_lshl_add_u64 v[218:219], s[22:23], 0, v[130:131]
	global_load_lds_dwordx4 v[218:219], off
	s_mov_b32 m0, s36
	s_nop 0
	global_load_lds_dwordx4 v[220:221], off
	s_waitcnt vmcnt(8) lgkmcnt(0)
	s_barrier
	v_mfma_f32_16x16x32_bf16 v[60:63], v[150:153], v[182:185], v[60:63]
	v_mfma_f32_16x16x32_bf16 v[56:59], v[158:161], v[182:185], v[56:59]
	v_mfma_f32_16x16x32_bf16 v[48:51], v[150:153], v[190:193], v[48:51]
	v_mfma_f32_16x16x32_bf16 v[40:43], v[158:161], v[190:193], v[40:43]
	v_mfma_f32_16x16x32_bf16 v[32:35], v[150:153], v[202:205], v[32:35]
	v_mfma_f32_16x16x32_bf16 v[24:27], v[158:161], v[202:205], v[24:27]
	v_mfma_f32_16x16x32_bf16 v[16:19], v[150:153], v[210:213], v[16:19]
	v_mfma_f32_16x16x32_bf16 v[8:11], v[158:161], v[210:213], v[8:11]
	v_mfma_f32_16x16x32_bf16 v[60:63], v[154:157], v[186:189], v[60:63]
	v_mfma_f32_16x16x32_bf16 v[56:59], v[162:165], v[186:189], v[56:59]
	v_mfma_f32_16x16x32_bf16 v[48:51], v[154:157], v[198:201], v[48:51]
	v_mfma_f32_16x16x32_bf16 v[40:43], v[162:165], v[198:201], v[40:43]
	v_mfma_f32_16x16x32_bf16 v[32:35], v[154:157], v[206:209], v[32:35]
	v_mfma_f32_16x16x32_bf16 v[24:27], v[162:165], v[206:209], v[24:27]
	v_mfma_f32_16x16x32_bf16 v[16:19], v[154:157], v[214:217], v[16:19]
	v_mfma_f32_16x16x32_bf16 v[8:11], v[162:165], v[214:217], v[8:11]
	v_mfma_f32_16x16x32_bf16 v[52:55], v[166:169], v[182:185], v[52:55]
	v_mfma_f32_16x16x32_bf16 v[44:47], v[174:177], v[182:185], v[44:47]
	v_mfma_f32_16x16x32_bf16 v[36:39], v[166:169], v[190:193], v[36:39]
	v_mfma_f32_16x16x32_bf16 v[28:31], v[174:177], v[190:193], v[28:31]
	v_mfma_f32_16x16x32_bf16 v[20:23], v[166:169], v[202:205], v[20:23]
	v_mfma_f32_16x16x32_bf16 v[12:15], v[174:177], v[202:205], v[12:15]
	v_mfma_f32_16x16x32_bf16 v[4:7], v[166:169], v[210:213], v[4:7]
	v_mfma_f32_16x16x32_bf16 v[0:3], v[174:177], v[210:213], v[0:3]
	v_mfma_f32_16x16x32_bf16 v[52:55], v[170:173], v[186:189], v[52:55]
	v_mfma_f32_16x16x32_bf16 v[44:47], v[178:181], v[186:189], v[44:47]
	v_mfma_f32_16x16x32_bf16 v[36:39], v[170:173], v[198:201], v[36:39]
	v_mfma_f32_16x16x32_bf16 v[28:31], v[178:181], v[198:201], v[28:31]
	v_mfma_f32_16x16x32_bf16 v[20:23], v[170:173], v[206:209], v[20:23]
	v_mfma_f32_16x16x32_bf16 v[12:15], v[178:181], v[206:209], v[12:15]
	v_mfma_f32_16x16x32_bf16 v[4:7], v[170:173], v[214:217], v[4:7]
	v_mfma_f32_16x16x32_bf16 v[0:3], v[178:181], v[214:217], v[0:3]
	s_barrier
	s_add_i32 s29, 0, 0x18000
	v_add_u32_e32 v128, s29, v147
	s_add_i32 s30, 0, 0x1c000
	ds_read_b128 v[150:153], v128
	ds_read_b128 v[154:157], v128 offset:1024
	ds_read_b128 v[158:161], v128 offset:2048
	ds_read_b128 v[162:165], v128 offset:3072
	v_add_u32_e32 v128, s30, v147
	ds_read_b128 v[166:169], v128
	ds_read_b128 v[170:173], v128 offset:1024
	ds_read_b128 v[174:177], v128 offset:2048
	ds_read_b128 v[178:181], v128 offset:3072
	s_add_u32 s2, s22, 0x20000
	s_addc_u32 s3, s23, 0
	s_mov_b32 m0, s37
	ds_read_b128 v[182:185], v148 offset:32768
	ds_read_b128 v[186:189], v148 offset:33792
	ds_read_b128 v[190:193], v148 offset:34816
	ds_read_b128 v[198:201], v148 offset:35840
	ds_read_b128 v[202:205], v148 offset:36864
	ds_read_b128 v[206:209], v148 offset:37888
	ds_read_b128 v[210:213], v148 offset:38912
	ds_read_b128 v[214:217], v148 offset:39936
	global_load_lds_dwordx4 v130, s[2:3]
	s_mov_b32 m0, s38
	s_nop 0
	global_load_lds_dwordx4 v134, s[2:3]
	s_waitcnt vmcnt(8) lgkmcnt(0)
	s_barrier
	v_mfma_f32_16x16x32_bf16 v[124:127], v[150:153], v[182:185], v[124:127]
	v_mfma_f32_16x16x32_bf16 v[120:123], v[158:161], v[182:185], v[120:123]
	v_mfma_f32_16x16x32_bf16 v[112:115], v[150:153], v[190:193], v[112:115]
	v_mfma_f32_16x16x32_bf16 v[104:107], v[158:161], v[190:193], v[104:107]
	v_mfma_f32_16x16x32_bf16 v[96:99], v[150:153], v[202:205], v[96:99]
	v_mfma_f32_16x16x32_bf16 v[88:91], v[158:161], v[202:205], v[88:91]
	v_mfma_f32_16x16x32_bf16 v[80:83], v[150:153], v[210:213], v[80:83]
	v_mfma_f32_16x16x32_bf16 v[72:75], v[158:161], v[210:213], v[72:75]
	v_mfma_f32_16x16x32_bf16 v[124:127], v[154:157], v[186:189], v[124:127]
	v_mfma_f32_16x16x32_bf16 v[120:123], v[162:165], v[186:189], v[120:123]
	v_mfma_f32_16x16x32_bf16 v[112:115], v[154:157], v[198:201], v[112:115]
	v_mfma_f32_16x16x32_bf16 v[104:107], v[162:165], v[198:201], v[104:107]
	v_mfma_f32_16x16x32_bf16 v[96:99], v[154:157], v[206:209], v[96:99]
	v_mfma_f32_16x16x32_bf16 v[88:91], v[162:165], v[206:209], v[88:91]
	v_mfma_f32_16x16x32_bf16 v[80:83], v[154:157], v[214:217], v[80:83]
	v_mfma_f32_16x16x32_bf16 v[72:75], v[162:165], v[214:217], v[72:75]
	v_mfma_f32_16x16x32_bf16 v[116:119], v[166:169], v[182:185], v[116:119]
	v_mfma_f32_16x16x32_bf16 v[108:111], v[174:177], v[182:185], v[108:111]
	v_mfma_f32_16x16x32_bf16 v[100:103], v[166:169], v[190:193], v[100:103]
	v_mfma_f32_16x16x32_bf16 v[92:95], v[174:177], v[190:193], v[92:95]
	v_mfma_f32_16x16x32_bf16 v[84:87], v[166:169], v[202:205], v[84:87]
	v_mfma_f32_16x16x32_bf16 v[76:79], v[174:177], v[202:205], v[76:79]
	v_mfma_f32_16x16x32_bf16 v[68:71], v[166:169], v[210:213], v[68:71]
	v_mfma_f32_16x16x32_bf16 v[64:67], v[174:177], v[210:213], v[64:67]
	v_mfma_f32_16x16x32_bf16 v[116:119], v[170:173], v[186:189], v[116:119]
	v_mfma_f32_16x16x32_bf16 v[108:111], v[178:181], v[186:189], v[108:111]
	v_mfma_f32_16x16x32_bf16 v[100:103], v[170:173], v[198:201], v[100:103]
	v_mfma_f32_16x16x32_bf16 v[92:95], v[178:181], v[198:201], v[92:95]
	v_mfma_f32_16x16x32_bf16 v[84:87], v[170:173], v[206:209], v[84:87]
	v_mfma_f32_16x16x32_bf16 v[76:79], v[178:181], v[206:209], v[76:79]
	v_mfma_f32_16x16x32_bf16 v[68:71], v[170:173], v[214:217], v[68:71]
	v_mfma_f32_16x16x32_bf16 v[64:67], v[178:181], v[214:217], v[64:67]
	s_barrier
	s_add_i32 s2, s29, s33
	v_lshl_add_u64 v[194:195], v[194:195], 0, s[42:43]
	s_mov_b32 m0, s2
	ds_read_b128 v[182:185], v148 offset:49152
	ds_read_b128 v[186:189], v148 offset:50176
	ds_read_b128 v[190:193], v148 offset:51200
	ds_read_b128 v[198:201], v148 offset:52224
	ds_read_b128 v[202:205], v148 offset:53248
	ds_read_b128 v[206:209], v148 offset:54272
	ds_read_b128 v[210:213], v148 offset:55296
	ds_read_b128 v[214:217], v148 offset:56320
	global_load_lds_dwordx4 v[194:195], off
	v_lshl_add_u64 v[194:195], v[196:197], 0, s[42:43]
	s_add_i32 m0, s2, 0x2000
	v_lshl_add_u64 v[144:145], v[144:145], 0, s[50:51]
	s_add_i32 s2, s30, s33
	global_load_lds_dwordx4 v[194:195], off
	v_lshl_add_u64 v[194:195], v[144:145], 0, v[132:133]
	s_mov_b32 m0, s2
	v_lshl_add_u64 v[144:145], v[144:145], 0, v[136:137]
	global_load_lds_dwordx4 v[194:195], off
	s_add_i32 m0, s2, 0x2000
	s_nop 0
	global_load_lds_dwordx4 v[144:145], off
	s_mov_b32 m0, s39
	v_lshl_add_u64 v[144:145], v[218:219], 0, s[42:43]
	global_load_lds_dwordx4 v[144:145], off
	s_mov_b32 m0, s53
	v_lshl_add_u64 v[144:145], v[220:221], 0, s[42:43]
	global_load_lds_dwordx4 v[144:145], off
	s_waitcnt vmcnt(8) lgkmcnt(0)
	s_barrier
	v_mfma_f32_16x16x32_bf16 v[60:63], v[150:153], v[182:185], v[60:63]
	v_mfma_f32_16x16x32_bf16 v[56:59], v[158:161], v[182:185], v[56:59]
	v_mfma_f32_16x16x32_bf16 v[48:51], v[150:153], v[190:193], v[48:51]
	v_mfma_f32_16x16x32_bf16 v[40:43], v[158:161], v[190:193], v[40:43]
	v_mfma_f32_16x16x32_bf16 v[32:35], v[150:153], v[202:205], v[32:35]
	v_mfma_f32_16x16x32_bf16 v[24:27], v[158:161], v[202:205], v[24:27]
	v_mfma_f32_16x16x32_bf16 v[16:19], v[150:153], v[210:213], v[16:19]
	v_mfma_f32_16x16x32_bf16 v[8:11], v[158:161], v[210:213], v[8:11]
	v_mfma_f32_16x16x32_bf16 v[60:63], v[154:157], v[186:189], v[60:63]
	v_mfma_f32_16x16x32_bf16 v[56:59], v[162:165], v[186:189], v[56:59]
	v_mfma_f32_16x16x32_bf16 v[48:51], v[154:157], v[198:201], v[48:51]
	v_mfma_f32_16x16x32_bf16 v[40:43], v[162:165], v[198:201], v[40:43]
	v_mfma_f32_16x16x32_bf16 v[32:35], v[154:157], v[206:209], v[32:35]
	v_mfma_f32_16x16x32_bf16 v[24:27], v[162:165], v[206:209], v[24:27]
	v_mfma_f32_16x16x32_bf16 v[16:19], v[154:157], v[214:217], v[16:19]
	v_mfma_f32_16x16x32_bf16 v[8:11], v[162:165], v[214:217], v[8:11]
	v_mfma_f32_16x16x32_bf16 v[52:55], v[166:169], v[182:185], v[52:55]
	v_mfma_f32_16x16x32_bf16 v[44:47], v[174:177], v[182:185], v[44:47]
	v_mfma_f32_16x16x32_bf16 v[36:39], v[166:169], v[190:193], v[36:39]
	v_mfma_f32_16x16x32_bf16 v[28:31], v[174:177], v[190:193], v[28:31]
	v_mfma_f32_16x16x32_bf16 v[20:23], v[166:169], v[202:205], v[20:23]
	v_mfma_f32_16x16x32_bf16 v[12:15], v[174:177], v[202:205], v[12:15]
	v_mfma_f32_16x16x32_bf16 v[4:7], v[166:169], v[210:213], v[4:7]
	v_mfma_f32_16x16x32_bf16 v[0:3], v[174:177], v[210:213], v[0:3]
	v_mfma_f32_16x16x32_bf16 v[52:55], v[170:173], v[186:189], v[52:55]
	v_mfma_f32_16x16x32_bf16 v[44:47], v[178:181], v[186:189], v[44:47]
	v_mfma_f32_16x16x32_bf16 v[36:39], v[170:173], v[198:201], v[36:39]
	v_mfma_f32_16x16x32_bf16 v[28:31], v[178:181], v[198:201], v[28:31]
	v_mfma_f32_16x16x32_bf16 v[20:23], v[170:173], v[206:209], v[20:23]
	v_mfma_f32_16x16x32_bf16 v[12:15], v[178:181], v[206:209], v[12:15]
	v_mfma_f32_16x16x32_bf16 v[4:7], v[170:173], v[214:217], v[4:7]
	v_mfma_f32_16x16x32_bf16 v[0:3], v[178:181], v[214:217], v[0:3]
	s_barrier
	s_add_i32 s2, s19, 2
	s_cmp_gt_u32 s19, 5
	s_mov_b32 s19, s2
	s_cbranch_scc1 .LBB0_1450
